# expert GEMM loops: B loads re-issued right after the bf16 conversions (LDS image write + A fragment reads moved after the issue)
# speedup vs baseline: 1.0913x; 1.0144x over previous
; #define PG8_BWAIT(n) asm volatile("s_waitcnt vmcnt(" #n ")" : "+v"(bv[0]), "+v"(bv[1]), "+v"(bv[2]), "+v"(bv[3]), "+v"(bv[4]), "+v"(bv[5]), "+v"(bv[6]), "+v"(bv[7]) :: "memory")
; #define PG8_STAGE_A(bufoff, V0, V1, kb) do { \
;         __builtin_amdgcn_global_load_lds((const unsigned*)((Abase + (kb)) + (V0)), (LAS unsigned*)(lds + (bufoff) + ldsw), 16, 0, 0); \
;         __builtin_amdgcn_global_load_lds((const unsigned*)((Abase + (kb)) + (V1)), (LAS unsigned*)(lds + (bufoff) + ldsw + 8192), 16, 0, 0); } while (0)
; #define PG8_LDA(dst, b, h) do { _Pragma("unroll") for (int m = 0; m < 4; ++m) _Pragma("unroll") for (int k = 0; k < 2; ++k) dst[m][k] = *(const LAS bf16x8*)(lds + PG8_SA(b, h) + aoff + m * 2048 + k * 1024); } while (0)
; #define PG8_LDB(dst, b, h) do { _Pragma("unroll") for (int n = 0; n < 2; ++n) _Pragma("unroll") for (int k = 0; k < 2; ++k) dst[n][k] = *(const LAS bf16x8*)(lds + PG8_SB(b, h) + boff + n * 2048 + k * 1024); } while (0)
; #define PG8_MMA(ai, bj, At, Bt) do { __builtin_amdgcn_s_setprio(1); _Pragma("unroll") for (int m = 0; m < 4; ++m) _Pragma("unroll") for (int n = 0; n < 2; ++n) _Pragma("unroll") for (int k = 0; k < 2; ++k) \
;         acc[ai][bj][m][n] = __builtin_amdgcn_mfma_f32_16x16x32_bf16(Bt[n][k], At[m][k], acc[ai][bj][m][n], 0, 0, 0); __builtin_amdgcn_s_setprio(0); } while (0)
; #define PG8_WAIT_V(n) asm volatile("s_waitcnt vmcnt(" #n ")" ::: "memory")
; #define PG8_WAIT_L(n) asm volatile("s_waitcnt lgkmcnt(" #n ")" ::: "memory")
; #define PG8_BAR __builtin_amdgcn_s_barrier()
; #define PG8_SCHED __builtin_amdgcn_sched_barrier(0)
; template <class Epi, class Sched, bool ALIGN_EPI>
; __device__ __forceinline__ void gemm_phase(LAS unsigned char* lds, const Gemm g, const Sched& S, const Epi& E) {
;     ...
;             PG8_LDB(B0, 0, 0); PG8_LDB(B1, 0, 1); PG8_SCHED; PG8_LDA(At, 0, 0); PG8_STAGE_A(PG8_SA(1, 1), vc10, vc11, kb1);
;             PG8_WAIT_V(12); PG8_WAIT_L(0); PG8_BAR; PG8_MMA(0, 0, At, B0); PG8_MMA(0, 1, At, B1); PG8_BAR; PG8_SCHED;
;             if (last) { vc10 = vn10; vc11 = vn11; }
;             PG8_BWAIT(2); PG8_BCOMMIT(0); PG8_SCHED; PG8_LDA(At, 0, 1); PG8_BISSUE(t + 3 >= nt ? pbn + (size_t)(t + 3 - nt) * 64 * Sched::LDN : pbc + (size_t)(t + 3) * 64 * Sched::LDN); PG8_STAGE_A(PG8_SA(0, 0), vc00, vc01, kb2);
.LBB0_2251:
	v_add_u32_e32 v162, 0x10000, v240
	v_add_u32_e32 v174, 0x14000, v240
	ds_read_b128 v[178:181], v162
	ds_read_b128 v[182:185], v162 offset:1024
	ds_read_b128 v[186:189], v162 offset:2048
	ds_read_b128 v[190:193], v162 offset:3072
	ds_read_b128 v[162:165], v174
	ds_read_b128 v[166:169], v174 offset:1024
	ds_read_b128 v[170:173], v174 offset:2048
	ds_read_b128 v[174:177], v174 offset:3072
	s_add_i32 s54, s53, 2
	s_add_i32 m0, s40, 0xc000
	s_add_u32 s4, s90, s22
	s_addc_u32 s5, s91, s23
	s_waitcnt lgkmcnt(0)
	ds_read_b128 v[194:197], v241
	ds_read_b128 v[198:201], v241 offset:1024
	ds_read_b128 v[202:205], v241 offset:2048
	ds_read_b128 v[206:209], v241 offset:3072
	ds_read_b128 v[210:213], v241 offset:4096
	ds_read_b128 v[214:217], v241 offset:5120
	ds_read_b128 v[218:221], v241 offset:6144
	ds_read_b128 v[222:225], v241 offset:7168
	global_load_lds_dwordx4 v234, s[4:5]
	s_add_i32 m0, s40, 0xe000
	s_nop 0
	global_load_lds_dwordx4 v235, s[4:5]
	s_waitcnt vmcnt(12)
	s_waitcnt lgkmcnt(0)
	s_barrier
	s_setprio 1
	s_waitcnt lgkmcnt(0)
	v_mfma_f32_16x16x32_bf16 v[158:161], v[178:181], v[194:197], v[158:161]
	v_mfma_f32_16x16x32_bf16 v[150:153], v[186:189], v[194:197], v[150:153]
	v_mfma_f32_16x16x32_bf16 v[142:145], v[178:181], v[202:205], v[142:145]
	v_mfma_f32_16x16x32_bf16 v[134:137], v[186:189], v[202:205], v[134:137]
	v_mfma_f32_16x16x32_bf16 v[126:129], v[178:181], v[210:213], v[126:129]
	v_mfma_f32_16x16x32_bf16 v[118:121], v[186:189], v[210:213], v[118:121]
	v_mfma_f32_16x16x32_bf16 v[110:113], v[178:181], v[218:221], v[110:113]
	v_mfma_f32_16x16x32_bf16 v[102:105], v[186:189], v[218:221], v[102:105]
	v_mfma_f32_16x16x32_bf16 v[158:161], v[182:185], v[198:201], v[158:161]
	v_mfma_f32_16x16x32_bf16 v[150:153], v[190:193], v[198:201], v[150:153]
	v_mfma_f32_16x16x32_bf16 v[142:145], v[182:185], v[206:209], v[142:145]
	v_mfma_f32_16x16x32_bf16 v[134:137], v[190:193], v[206:209], v[134:137]
	v_mfma_f32_16x16x32_bf16 v[126:129], v[182:185], v[214:217], v[126:129]
	v_mfma_f32_16x16x32_bf16 v[118:121], v[190:193], v[214:217], v[118:121]
	v_mfma_f32_16x16x32_bf16 v[110:113], v[182:185], v[222:225], v[110:113]
	v_mfma_f32_16x16x32_bf16 v[102:105], v[190:193], v[222:225], v[102:105]
	s_setprio 0
	s_setprio 1
	v_mfma_f32_16x16x32_bf16 v[154:157], v[162:165], v[194:197], v[154:157]
	v_mfma_f32_16x16x32_bf16 v[146:149], v[170:173], v[194:197], v[146:149]
	v_mfma_f32_16x16x32_bf16 v[138:141], v[162:165], v[202:205], v[138:141]
	v_mfma_f32_16x16x32_bf16 v[130:133], v[170:173], v[202:205], v[130:133]
	v_mfma_f32_16x16x32_bf16 v[122:125], v[162:165], v[210:213], v[122:125]
	v_mfma_f32_16x16x32_bf16 v[114:117], v[170:173], v[210:213], v[114:117]
	v_mfma_f32_16x16x32_bf16 v[106:109], v[162:165], v[218:221], v[106:109]
	v_mfma_f32_16x16x32_bf16 v[98:101], v[170:173], v[218:221], v[98:101]
	v_mfma_f32_16x16x32_bf16 v[154:157], v[166:169], v[198:201], v[154:157]
	v_mfma_f32_16x16x32_bf16 v[146:149], v[174:177], v[198:201], v[146:149]
	v_mfma_f32_16x16x32_bf16 v[138:141], v[166:169], v[206:209], v[138:141]
	v_mfma_f32_16x16x32_bf16 v[130:133], v[174:177], v[206:209], v[130:133]
	v_mfma_f32_16x16x32_bf16 v[122:125], v[166:169], v[214:217], v[122:125]
	v_mfma_f32_16x16x32_bf16 v[114:117], v[174:177], v[214:217], v[114:117]
	v_mfma_f32_16x16x32_bf16 v[106:109], v[166:169], v[222:225], v[106:109]
	v_mfma_f32_16x16x32_bf16 v[98:101], v[174:177], v[222:225], v[98:101]
	s_setprio 0
	s_barrier
	s_waitcnt vmcnt(2)
	s_nop 0
	v_add_u32_e32 v210, 0x10000, v232
	v_cvt_pk_bf16_f32 v194, v2, v6
	v_cvt_pk_bf16_f32 v195, v10, v14
	v_cvt_pk_bf16_f32 v196, v18, v22
	v_cvt_pk_bf16_f32 v197, v26, v30
	v_cvt_pk_bf16_f32 v198, v3, v7
	v_cvt_pk_bf16_f32 v199, v11, v15
	v_cvt_pk_bf16_f32 v200, v19, v23
	v_cvt_pk_bf16_f32 v201, v27, v31
	v_cvt_pk_bf16_f32 v202, v4, v8
	v_cvt_pk_bf16_f32 v203, v12, v16
	v_cvt_pk_bf16_f32 v204, v20, v24
	v_cvt_pk_bf16_f32 v205, v28, v32
	v_cvt_pk_bf16_f32 v206, v5, v9
	v_cvt_pk_bf16_f32 v207, v13, v17
	v_cvt_pk_bf16_f32 v208, v21, v25
	v_cvt_pk_bf16_f32 v209, v29, v33
	v_xor_b32_e32 v211, 64, v210
	v_xor_b32_e32 v212, 0x80, v210
	v_xor_b32_e32 v213, 0xc0, v210
	s_cmp_lt_u32 s54, 13
	s_mov_b64 s[6:7], -1
	s_cbranch_scc0 .LBB0_2253
	s_add_u32 s4, s20, 0x30000
	s_addc_u32 s5, s21, 0
	s_mov_b64 s[6:7], 0

; #define PG8_BWAIT(n) asm volatile("s_waitcnt vmcnt(" #n ")" : "+v"(bv[0]), "+v"(bv[1]), "+v"(bv[2]), "+v"(bv[3]), "+v"(bv[4]), "+v"(bv[5]), "+v"(bv[6]), "+v"(bv[7]) :: "memory")
; #define PG8_STAGE_A(bufoff, V0, V1, kb) do { \
;         __builtin_amdgcn_global_load_lds((const unsigned*)((Abase + (kb)) + (V0)), (LAS unsigned*)(lds + (bufoff) + ldsw), 16, 0, 0); \
;         __builtin_amdgcn_global_load_lds((const unsigned*)((Abase + (kb)) + (V1)), (LAS unsigned*)(lds + (bufoff) + ldsw + 8192), 16, 0, 0); } while (0)
; #define PG8_LDA(dst, b, h) do { _Pragma("unroll") for (int m = 0; m < 4; ++m) _Pragma("unroll") for (int k = 0; k < 2; ++k) dst[m][k] = *(const LAS bf16x8*)(lds + PG8_SA(b, h) + aoff + m * 2048 + k * 1024); } while (0)
; #define PG8_MMA(ai, bj, At, Bt) do { __builtin_amdgcn_s_setprio(1); _Pragma("unroll") for (int m = 0; m < 4; ++m) _Pragma("unroll") for (int n = 0; n < 2; ++n) _Pragma("unroll") for (int k = 0; k < 2; ++k) \
;         acc[ai][bj][m][n] = __builtin_amdgcn_mfma_f32_16x16x32_bf16(Bt[n][k], At[m][k], acc[ai][bj][m][n], 0, 0, 0); __builtin_amdgcn_s_setprio(0); } while (0)
; #define PG8_WAIT_V(n) asm volatile("s_waitcnt vmcnt(" #n ")" ::: "memory")
; #define PG8_WAIT_L(n) asm volatile("s_waitcnt lgkmcnt(" #n ")" ::: "memory")
; #define PG8_BAR __builtin_amdgcn_s_barrier()
; #define PG8_SCHED __builtin_amdgcn_sched_barrier(0)
; template <class Epi, class Sched, bool ALIGN_EPI>
; __device__ __forceinline__ void gemm_phase(LAS unsigned char* lds, const Gemm g, const Sched& S, const Epi& E) {
;     ...
;             PG8_BWAIT(2); PG8_BCOMMIT(0); PG8_SCHED; PG8_LDA(At, 0, 1); PG8_BISSUE(t + 3 >= nt ? pbn + (size_t)(t + 3 - nt) * 64 * Sched::LDN : pbc + (size_t)(t + 3) * 64 * Sched::LDN); PG8_STAGE_A(PG8_SA(0, 0), vc00, vc01, kb2);
;             PG8_WAIT_V(12); PG8_WAIT_L(0); PG8_BAR; if (half1) { PG8_MMA(1, 0, At, B0); PG8_MMA(1, 1, At, B1); } PG8_BAR; PG8_SCHED;
.LBB0_2255:
	s_add_i32 s2, s22, 0xe8940080
	s_cmp_eq_u32 s53, 12
	global_load_dwordx4 v[2:5], v231, s[4:5] offset:0
	s_cselect_b64 s[6:7], -1, 0
	global_load_dwordx4 v[6:9], v231, s[4:5] offset:0x400
	s_and_b64 s[26:27], s[6:7], exec
	global_load_dwordx4 v[10:13], v231, s[4:5] offset:0x800
	s_cselect_b32 s2, 0, s2
	global_load_dwordx4 v[14:17], v231, s[4:5] offset:0xc00
	s_add_u32 s4, s4, 0x1000
	s_addc_u32 s5, s5, 0
	global_load_dwordx4 v[18:21], v231, s[4:5] offset:0
	global_load_dwordx4 v[22:25], v231, s[4:5] offset:0x400
	global_load_dwordx4 v[26:29], v231, s[4:5] offset:0x800
	global_load_dwordx4 v[30:33], v231, s[4:5] offset:0xc00
	ds_write_b128 v210, v[194:197]
	ds_write_b128 v211, v[198:201]
	ds_write_b128 v212, v[202:205]
	ds_write_b128 v213, v[206:209]
	ds_read_b128 v[218:221], v241 offset:16384
	ds_read_b128 v[222:225], v241 offset:17408
	ds_read_b128 v[210:213], v241 offset:18432
	ds_read_b128 v[214:217], v241 offset:19456
	ds_read_b128 v[202:205], v241 offset:20480
	ds_read_b128 v[206:209], v241 offset:21504
	ds_read_b128 v[194:197], v241 offset:22528
	ds_read_b128 v[198:201], v241 offset:23552
	v_readlane_b32 s4, v255, 13
	v_readlane_b32 s5, v255, 14
	s_add_u32 s26, s4, s2
	s_mov_b32 m0, s40
	v_cndmask_b32_e64 v226, v226, v242, s[6:7]
	s_addc_u32 s27, s5, 0
	v_cndmask_b32_e64 v228, v228, v243, s[6:7]
	global_load_lds_dwordx4 v226, s[26:27]
	s_mov_b32 m0, s41
	v_cndmask_b32_e64 v229, 0, 1, s[24:25]
	global_load_lds_dwordx4 v228, s[26:27]
	s_waitcnt vmcnt(12)
	s_waitcnt lgkmcnt(0)
	v_cmp_ne_u32_e64 s[4:5], 1, v229
	s_andn2_b64 vcc, exec, s[24:25]
	s_barrier
	s_cbranch_vccnz .LBB0_2257
	s_setprio 1
	s_waitcnt lgkmcnt(0)
	v_mfma_f32_16x16x32_bf16 v[94:97], v[178:181], v[218:221], v[94:97]
	v_mfma_f32_16x16x32_bf16 v[86:89], v[186:189], v[218:221], v[86:89]
	v_mfma_f32_16x16x32_bf16 v[78:81], v[178:181], v[210:213], v[78:81]
	v_mfma_f32_16x16x32_bf16 v[70:73], v[186:189], v[210:213], v[70:73]
	v_mfma_f32_16x16x32_bf16 v[62:65], v[178:181], v[202:205], v[62:65]
	v_mfma_f32_16x16x32_bf16 v[54:57], v[186:189], v[202:205], v[54:57]
	v_mfma_f32_16x16x32_bf16 v[46:49], v[178:181], v[194:197], v[46:49]
	v_mfma_f32_16x16x32_bf16 v[38:41], v[186:189], v[194:197], v[38:41]
	v_mfma_f32_16x16x32_bf16 v[94:97], v[182:185], v[222:225], v[94:97]
	v_mfma_f32_16x16x32_bf16 v[86:89], v[190:193], v[222:225], v[86:89]
	v_mfma_f32_16x16x32_bf16 v[78:81], v[182:185], v[214:217], v[78:81]
	v_mfma_f32_16x16x32_bf16 v[70:73], v[190:193], v[214:217], v[70:73]
	v_mfma_f32_16x16x32_bf16 v[62:65], v[182:185], v[206:209], v[62:65]
	v_mfma_f32_16x16x32_bf16 v[54:57], v[190:193], v[206:209], v[54:57]
	v_mfma_f32_16x16x32_bf16 v[46:49], v[182:185], v[198:201], v[46:49]
	v_mfma_f32_16x16x32_bf16 v[38:41], v[190:193], v[198:201], v[38:41]
	s_setprio 0
	s_setprio 1
	v_mfma_f32_16x16x32_bf16 v[90:93], v[162:165], v[218:221], v[90:93]
	v_mfma_f32_16x16x32_bf16 v[82:85], v[170:173], v[218:221], v[82:85]
	v_mfma_f32_16x16x32_bf16 v[74:77], v[162:165], v[210:213], v[74:77]
	v_mfma_f32_16x16x32_bf16 v[66:69], v[170:173], v[210:213], v[66:69]
	v_mfma_f32_16x16x32_bf16 v[58:61], v[162:165], v[202:205], v[58:61]
	v_mfma_f32_16x16x32_bf16 v[50:53], v[170:173], v[202:205], v[50:53]
	v_mfma_f32_16x16x32_bf16 v[42:45], v[162:165], v[194:197], v[42:45]
	v_mfma_f32_16x16x32_bf16 v[34:37], v[170:173], v[194:197], v[34:37]
	v_mfma_f32_16x16x32_bf16 v[90:93], v[166:169], v[222:225], v[90:93]
	v_mfma_f32_16x16x32_bf16 v[82:85], v[174:177], v[222:225], v[82:85]
	v_mfma_f32_16x16x32_bf16 v[74:77], v[166:169], v[214:217], v[74:77]
	v_mfma_f32_16x16x32_bf16 v[66:69], v[174:177], v[214:217], v[66:69]
	v_mfma_f32_16x16x32_bf16 v[58:61], v[166:169], v[206:209], v[58:61]
	v_mfma_f32_16x16x32_bf16 v[50:53], v[174:177], v[206:209], v[50:53]
	v_mfma_f32_16x16x32_bf16 v[42:45], v[166:169], v[198:201], v[42:45]
	v_mfma_f32_16x16x32_bf16 v[34:37], v[174:177], v[198:201], v[34:37]
	s_setprio 0
; #define PG8_BWAIT(n) asm volatile("s_waitcnt vmcnt(" #n ")" : "+v"(bv[0]), "+v"(bv[1]), "+v"(bv[2]), "+v"(bv[3]), "+v"(bv[4]), "+v"(bv[5]), "+v"(bv[6]), "+v"(bv[7]) :: "memory")
; #define PG8_STAGE_A(bufoff, V0, V1, kb) do { \
;         __builtin_amdgcn_global_load_lds((const unsigned*)((Abase + (kb)) + (V0)), (LAS unsigned*)(lds + (bufoff) + ldsw), 16, 0, 0); \
;         __builtin_amdgcn_global_load_lds((const unsigned*)((Abase + (kb)) + (V1)), (LAS unsigned*)(lds + (bufoff) + ldsw + 8192), 16, 0, 0); } while (0)
; #define PG8_LDA(dst, b, h) do { _Pragma("unroll") for (int m = 0; m < 4; ++m) _Pragma("unroll") for (int k = 0; k < 2; ++k) dst[m][k] = *(const LAS bf16x8*)(lds + PG8_SA(b, h) + aoff + m * 2048 + k * 1024); } while (0)
; #define PG8_LDB(dst, b, h) do { _Pragma("unroll") for (int n = 0; n < 2; ++n) _Pragma("unroll") for (int k = 0; k < 2; ++k) dst[n][k] = *(const LAS bf16x8*)(lds + PG8_SB(b, h) + boff + n * 2048 + k * 1024); } while (0)
; #define PG8_MMA(ai, bj, At, Bt) do { __builtin_amdgcn_s_setprio(1); _Pragma("unroll") for (int m = 0; m < 4; ++m) _Pragma("unroll") for (int n = 0; n < 2; ++n) _Pragma("unroll") for (int k = 0; k < 2; ++k) \
;         acc[ai][bj][m][n] = __builtin_amdgcn_mfma_f32_16x16x32_bf16(Bt[n][k], At[m][k], acc[ai][bj][m][n], 0, 0, 0); __builtin_amdgcn_s_setprio(0); } while (0)
; #define PG8_WAIT_V(n) asm volatile("s_waitcnt vmcnt(" #n ")" ::: "memory")
; #define PG8_WAIT_L(n) asm volatile("s_waitcnt lgkmcnt(" #n ")" ::: "memory")
; #define PG8_BAR __builtin_amdgcn_s_barrier()
; #define PG8_SCHED __builtin_amdgcn_sched_barrier(0)
; template <class Epi, class Sched, bool ALIGN_EPI>
; __device__ __forceinline__ void gemm_phase(LAS unsigned char* lds, const Gemm g, const Sched& S, const Epi& E) {
;     ...
;             PG8_LDB(B0, 1, 0); PG8_LDB(B1, 1, 1); PG8_SCHED; PG8_LDA(At, 1, 0); PG8_STAGE_A(PG8_SA(0, 1), vc10, vc11, kb2);
;             PG8_WAIT_V(12); PG8_WAIT_L(0); PG8_BAR; PG8_MMA(0, 0, At, B0); PG8_MMA(0, 1, At, B1); PG8_BAR; PG8_SCHED;
;             PG8_BWAIT(2); PG8_BCOMMIT(1); PG8_SCHED; PG8_LDA(At, 1, 1); PG8_BISSUE(t + 4 >= nt ? pbn + (size_t)(t + 4 - nt) * 64 * Sched::LDN : pbc + (size_t)(t + 4) * 64 * Sched::LDN); PG8_STAGE_A(PG8_SA(1, 0), vc00, vc01, kb2 + 128u);
.LBB0_2257:
	v_cndmask_b32_e64 v235, v235, v245, s[6:7]
	v_cndmask_b32_e64 v234, v234, v244, s[6:7]
	s_barrier
	v_add_u32_e32 v162, 0x18000, v240
	v_add_u32_e32 v174, 0x1c000, v240
	ds_read_b128 v[178:181], v162
	ds_read_b128 v[182:185], v162 offset:1024
	ds_read_b128 v[186:189], v162 offset:2048
	ds_read_b128 v[190:193], v162 offset:3072
	ds_read_b128 v[162:165], v174
	ds_read_b128 v[166:169], v174 offset:1024
	ds_read_b128 v[170:173], v174 offset:2048
	ds_read_b128 v[174:177], v174 offset:3072
	s_mov_b32 m0, s42
	s_waitcnt lgkmcnt(0)
	ds_read_b128 v[194:197], v241 offset:32768
	ds_read_b128 v[198:201], v241 offset:33792
	ds_read_b128 v[202:205], v241 offset:34816
	ds_read_b128 v[206:209], v241 offset:35840
	ds_read_b128 v[210:213], v241 offset:36864
	ds_read_b128 v[214:217], v241 offset:37888
	ds_read_b128 v[218:221], v241 offset:38912
	ds_read_b128 v[222:225], v241 offset:39936
	global_load_lds_dwordx4 v234, s[26:27]
	s_mov_b32 m0, s43
	s_nop 0
	global_load_lds_dwordx4 v235, s[26:27]
	s_waitcnt vmcnt(12)
	s_waitcnt lgkmcnt(0)
	s_barrier
	s_setprio 1
	s_waitcnt lgkmcnt(0)
	v_mfma_f32_16x16x32_bf16 v[158:161], v[178:181], v[194:197], v[158:161]
	v_mfma_f32_16x16x32_bf16 v[150:153], v[186:189], v[194:197], v[150:153]
	v_mfma_f32_16x16x32_bf16 v[142:145], v[178:181], v[202:205], v[142:145]
	v_mfma_f32_16x16x32_bf16 v[134:137], v[186:189], v[202:205], v[134:137]
	v_mfma_f32_16x16x32_bf16 v[126:129], v[178:181], v[210:213], v[126:129]
	v_mfma_f32_16x16x32_bf16 v[118:121], v[186:189], v[210:213], v[118:121]
	v_mfma_f32_16x16x32_bf16 v[110:113], v[178:181], v[218:221], v[110:113]
	v_mfma_f32_16x16x32_bf16 v[102:105], v[186:189], v[218:221], v[102:105]
	v_mfma_f32_16x16x32_bf16 v[158:161], v[182:185], v[198:201], v[158:161]
	v_mfma_f32_16x16x32_bf16 v[150:153], v[190:193], v[198:201], v[150:153]
	v_mfma_f32_16x16x32_bf16 v[142:145], v[182:185], v[206:209], v[142:145]
	v_mfma_f32_16x16x32_bf16 v[134:137], v[190:193], v[206:209], v[134:137]
	v_mfma_f32_16x16x32_bf16 v[126:129], v[182:185], v[214:217], v[126:129]
	v_mfma_f32_16x16x32_bf16 v[118:121], v[190:193], v[214:217], v[118:121]
	v_mfma_f32_16x16x32_bf16 v[110:113], v[182:185], v[222:225], v[110:113]
	v_mfma_f32_16x16x32_bf16 v[102:105], v[190:193], v[222:225], v[102:105]
	s_setprio 0
	s_setprio 1
	v_mfma_f32_16x16x32_bf16 v[154:157], v[162:165], v[194:197], v[154:157]
	v_mfma_f32_16x16x32_bf16 v[146:149], v[170:173], v[194:197], v[146:149]
	v_mfma_f32_16x16x32_bf16 v[138:141], v[162:165], v[202:205], v[138:141]
	v_mfma_f32_16x16x32_bf16 v[130:133], v[170:173], v[202:205], v[130:133]
	v_mfma_f32_16x16x32_bf16 v[122:125], v[162:165], v[210:213], v[122:125]
	v_mfma_f32_16x16x32_bf16 v[114:117], v[170:173], v[210:213], v[114:117]
	v_mfma_f32_16x16x32_bf16 v[106:109], v[162:165], v[218:221], v[106:109]
	v_mfma_f32_16x16x32_bf16 v[98:101], v[170:173], v[218:221], v[98:101]
	v_mfma_f32_16x16x32_bf16 v[154:157], v[166:169], v[198:201], v[154:157]
	v_mfma_f32_16x16x32_bf16 v[146:149], v[174:177], v[198:201], v[146:149]
	v_mfma_f32_16x16x32_bf16 v[138:141], v[166:169], v[206:209], v[138:141]
	v_mfma_f32_16x16x32_bf16 v[130:133], v[174:177], v[206:209], v[130:133]
	v_mfma_f32_16x16x32_bf16 v[122:125], v[166:169], v[214:217], v[122:125]
	v_mfma_f32_16x16x32_bf16 v[114:117], v[174:177], v[214:217], v[114:117]
	v_mfma_f32_16x16x32_bf16 v[106:109], v[166:169], v[222:225], v[106:109]
	v_mfma_f32_16x16x32_bf16 v[98:101], v[174:177], v[222:225], v[98:101]
	s_setprio 0
	s_barrier
	s_waitcnt vmcnt(2)
	s_nop 0
	v_add_u32_e32 v210, 0x18000, v232
	v_cvt_pk_bf16_f32 v194, v2, v6
	v_cvt_pk_bf16_f32 v195, v10, v14
	v_cvt_pk_bf16_f32 v196, v18, v22
	v_cvt_pk_bf16_f32 v197, v26, v30
	v_cvt_pk_bf16_f32 v198, v3, v7
	v_cvt_pk_bf16_f32 v199, v11, v15
	v_cvt_pk_bf16_f32 v200, v19, v23
	v_cvt_pk_bf16_f32 v201, v27, v31
	v_cvt_pk_bf16_f32 v202, v4, v8
	v_cvt_pk_bf16_f32 v203, v12, v16
	v_cvt_pk_bf16_f32 v204, v20, v24
	v_cvt_pk_bf16_f32 v205, v28, v32
	v_cvt_pk_bf16_f32 v206, v5, v9
	v_cvt_pk_bf16_f32 v207, v13, v17
	v_cvt_pk_bf16_f32 v208, v21, v25
	v_cvt_pk_bf16_f32 v209, v29, v33
	v_xor_b32_e32 v211, 64, v210
	v_xor_b32_e32 v212, 0x80, v210
	v_xor_b32_e32 v213, 0xc0, v210
	s_cmp_lt_u32 s54, 12
	s_mov_b64 s[28:29], -1
	s_cbranch_scc0 .LBB0_2259
	s_add_u32 s6, s20, 0x40000
	s_addc_u32 s7, s21, 0
	s_mov_b64 s[28:29], 0

; #define PG8_BWAIT(n) asm volatile("s_waitcnt vmcnt(" #n ")" : "+v"(bv[0]), "+v"(bv[1]), "+v"(bv[2]), "+v"(bv[3]), "+v"(bv[4]), "+v"(bv[5]), "+v"(bv[6]), "+v"(bv[7]) :: "memory")
; #define PG8_STAGE_A(bufoff, V0, V1, kb) do { \
;         __builtin_amdgcn_global_load_lds((const unsigned*)((Abase + (kb)) + (V0)), (LAS unsigned*)(lds + (bufoff) + ldsw), 16, 0, 0); \
;         __builtin_amdgcn_global_load_lds((const unsigned*)((Abase + (kb)) + (V1)), (LAS unsigned*)(lds + (bufoff) + ldsw + 8192), 16, 0, 0); } while (0)
; #define PG8_LDA(dst, b, h) do { _Pragma("unroll") for (int m = 0; m < 4; ++m) _Pragma("unroll") for (int k = 0; k < 2; ++k) dst[m][k] = *(const LAS bf16x8*)(lds + PG8_SA(b, h) + aoff + m * 2048 + k * 1024); } while (0)
; #define PG8_MMA(ai, bj, At, Bt) do { __builtin_amdgcn_s_setprio(1); _Pragma("unroll") for (int m = 0; m < 4; ++m) _Pragma("unroll") for (int n = 0; n < 2; ++n) _Pragma("unroll") for (int k = 0; k < 2; ++k) \
;         acc[ai][bj][m][n] = __builtin_amdgcn_mfma_f32_16x16x32_bf16(Bt[n][k], At[m][k], acc[ai][bj][m][n], 0, 0, 0); __builtin_amdgcn_s_setprio(0); } while (0)
; #define PG8_WAIT_V(n) asm volatile("s_waitcnt vmcnt(" #n ")" ::: "memory")
; #define PG8_WAIT_L(n) asm volatile("s_waitcnt lgkmcnt(" #n ")" ::: "memory")
; #define PG8_BAR __builtin_amdgcn_s_barrier()
; #define PG8_SCHED __builtin_amdgcn_sched_barrier(0)
; template <class Epi, class Sched, bool ALIGN_EPI>
; __device__ __forceinline__ void gemm_phase(LAS unsigned char* lds, const Gemm g, const Sched& S, const Epi& E) {
;     ...
;             PG8_BWAIT(2); PG8_BCOMMIT(1); PG8_SCHED; PG8_LDA(At, 1, 1); PG8_BISSUE(t + 4 >= nt ? pbn + (size_t)(t + 4 - nt) * 64 * Sched::LDN : pbc + (size_t)(t + 4) * 64 * Sched::LDN); PG8_STAGE_A(PG8_SA(1, 0), vc00, vc01, kb2 + 128u);
;             PG8_WAIT_V(12); PG8_WAIT_L(0); PG8_BAR; if (half1) { PG8_MMA(1, 0, At, B0); PG8_MMA(1, 1, At, B1); } PG8_BAR; PG8_SCHED;
.LBB0_2261:
	global_load_dwordx4 v[2:5], v231, s[6:7] offset:0
	global_load_dwordx4 v[6:9], v231, s[6:7] offset:0x400
	global_load_dwordx4 v[10:13], v231, s[6:7] offset:0x800
	global_load_dwordx4 v[14:17], v231, s[6:7] offset:0xc00
	s_add_u32 s6, s6, 0x1000
	s_addc_u32 s7, s7, 0
	global_load_dwordx4 v[18:21], v231, s[6:7] offset:0
	global_load_dwordx4 v[22:25], v231, s[6:7] offset:0x400
	v_lshl_add_u64 v[246:247], s[26:27], 0, v[226:227]
	v_mov_b32_e32 v229, v227
	global_load_dwordx4 v[26:29], v231, s[6:7] offset:0x800
	s_mov_b32 m0, s44
	v_lshl_add_u64 v[248:249], s[26:27], 0, v[228:229]
	global_load_dwordx4 v[30:33], v231, s[6:7] offset:0xc00
	ds_write_b128 v210, v[194:197]
	ds_write_b128 v211, v[198:201]
	ds_write_b128 v212, v[202:205]
	ds_write_b128 v213, v[206:209]
	ds_read_b128 v[218:221], v241 offset:49152
	ds_read_b128 v[222:225], v241 offset:50176
	ds_read_b128 v[210:213], v241 offset:51200
	ds_read_b128 v[214:217], v241 offset:52224
	ds_read_b128 v[202:205], v241 offset:53248
	ds_read_b128 v[206:209], v241 offset:54272
	ds_read_b128 v[194:197], v241 offset:55296
	ds_read_b128 v[198:201], v241 offset:56320
	v_lshl_add_u64 v[246:247], v[246:247], 0, s[12:13]
	global_load_lds_dwordx4 v[246:247], off
	v_lshl_add_u64 v[246:247], v[248:249], 0, s[12:13]
	s_mov_b32 m0, s45
	s_and_b64 vcc, exec, s[4:5]
	global_load_lds_dwordx4 v[246:247], off
	s_waitcnt vmcnt(12)
	s_waitcnt lgkmcnt(0)
	s_barrier
	s_cbranch_vccnz .LBB0_2263
	s_setprio 1
	s_waitcnt lgkmcnt(0)
	v_mfma_f32_16x16x32_bf16 v[94:97], v[178:181], v[218:221], v[94:97]
	v_mfma_f32_16x16x32_bf16 v[86:89], v[186:189], v[218:221], v[86:89]
	v_mfma_f32_16x16x32_bf16 v[78:81], v[178:181], v[210:213], v[78:81]
	v_mfma_f32_16x16x32_bf16 v[70:73], v[186:189], v[210:213], v[70:73]
	v_mfma_f32_16x16x32_bf16 v[62:65], v[178:181], v[202:205], v[62:65]
	v_mfma_f32_16x16x32_bf16 v[54:57], v[186:189], v[202:205], v[54:57]
	v_mfma_f32_16x16x32_bf16 v[46:49], v[178:181], v[194:197], v[46:49]
	v_mfma_f32_16x16x32_bf16 v[38:41], v[186:189], v[194:197], v[38:41]
	v_mfma_f32_16x16x32_bf16 v[94:97], v[182:185], v[222:225], v[94:97]
	v_mfma_f32_16x16x32_bf16 v[86:89], v[190:193], v[222:225], v[86:89]
	v_mfma_f32_16x16x32_bf16 v[78:81], v[182:185], v[214:217], v[78:81]
	v_mfma_f32_16x16x32_bf16 v[70:73], v[190:193], v[214:217], v[70:73]
	v_mfma_f32_16x16x32_bf16 v[62:65], v[182:185], v[206:209], v[62:65]
	v_mfma_f32_16x16x32_bf16 v[54:57], v[190:193], v[206:209], v[54:57]
	v_mfma_f32_16x16x32_bf16 v[46:49], v[182:185], v[198:201], v[46:49]
	v_mfma_f32_16x16x32_bf16 v[38:41], v[190:193], v[198:201], v[38:41]
	s_setprio 0
	s_setprio 1
	v_mfma_f32_16x16x32_bf16 v[90:93], v[162:165], v[218:221], v[90:93]
	v_mfma_f32_16x16x32_bf16 v[82:85], v[170:173], v[218:221], v[82:85]
	v_mfma_f32_16x16x32_bf16 v[74:77], v[162:165], v[210:213], v[74:77]
	v_mfma_f32_16x16x32_bf16 v[66:69], v[170:173], v[210:213], v[66:69]
	v_mfma_f32_16x16x32_bf16 v[58:61], v[162:165], v[202:205], v[58:61]
	v_mfma_f32_16x16x32_bf16 v[50:53], v[170:173], v[202:205], v[50:53]
	v_mfma_f32_16x16x32_bf16 v[42:45], v[162:165], v[194:197], v[42:45]
	v_mfma_f32_16x16x32_bf16 v[34:37], v[170:173], v[194:197], v[34:37]
	v_mfma_f32_16x16x32_bf16 v[90:93], v[166:169], v[222:225], v[90:93]
	v_mfma_f32_16x16x32_bf16 v[82:85], v[174:177], v[222:225], v[82:85]
	v_mfma_f32_16x16x32_bf16 v[74:77], v[166:169], v[214:217], v[74:77]
	v_mfma_f32_16x16x32_bf16 v[66:69], v[174:177], v[214:217], v[66:69]
	v_mfma_f32_16x16x32_bf16 v[58:61], v[166:169], v[206:209], v[58:61]
	v_mfma_f32_16x16x32_bf16 v[50:53], v[174:177], v[206:209], v[50:53]
	v_mfma_f32_16x16x32_bf16 v[42:45], v[166:169], v[198:201], v[42:45]
	v_mfma_f32_16x16x32_bf16 v[34:37], v[174:177], v[198:201], v[34:37]
	s_setprio 0

; #define PG8_BWAIT(n) asm volatile("s_waitcnt vmcnt(" #n ")" : "+v"(bv[0]), "+v"(bv[1]), "+v"(bv[2]), "+v"(bv[3]), "+v"(bv[4]), "+v"(bv[5]), "+v"(bv[6]), "+v"(bv[7]) :: "memory")
; #define PG8_STAGE_A(bufoff, V0, V1, kb) do { \
;         __builtin_amdgcn_global_load_lds((const unsigned*)((Abase + (kb)) + (V0)), (LAS unsigned*)(lds + (bufoff) + ldsw), 16, 0, 0); \
;         __builtin_amdgcn_global_load_lds((const unsigned*)((Abase + (kb)) + (V1)), (LAS unsigned*)(lds + (bufoff) + ldsw + 8192), 16, 0, 0); } while (0)
; #define PG8_LDA(dst, b, h) do { _Pragma("unroll") for (int m = 0; m < 4; ++m) _Pragma("unroll") for (int k = 0; k < 2; ++k) dst[m][k] = *(const LAS bf16x8*)(lds + PG8_SA(b, h) + aoff + m * 2048 + k * 1024); } while (0)
; #define PG8_LDB(dst, b, h) do { _Pragma("unroll") for (int n = 0; n < 2; ++n) _Pragma("unroll") for (int k = 0; k < 2; ++k) dst[n][k] = *(const LAS bf16x8*)(lds + PG8_SB(b, h) + boff + n * 2048 + k * 1024); } while (0)
; #define PG8_MMA(ai, bj, At, Bt) do { __builtin_amdgcn_s_setprio(1); _Pragma("unroll") for (int m = 0; m < 4; ++m) _Pragma("unroll") for (int n = 0; n < 2; ++n) _Pragma("unroll") for (int k = 0; k < 2; ++k) \
;         acc[ai][bj][m][n] = __builtin_amdgcn_mfma_f32_16x16x32_bf16(Bt[n][k], At[m][k], acc[ai][bj][m][n], 0, 0, 0); __builtin_amdgcn_s_setprio(0); } while (0)
; #define PG8_WAIT_V(n) asm volatile("s_waitcnt vmcnt(" #n ")" ::: "memory")
; #define PG8_WAIT_L(n) asm volatile("s_waitcnt lgkmcnt(" #n ")" ::: "memory")
; #define PG8_BAR __builtin_amdgcn_s_barrier()
; template <class Epi, class Sched, bool ALIGN_EPI>
; __device__ __forceinline__ void gemm_phase(LAS unsigned char* lds, const Gemm g, const Sched& S, const Epi& E) {
;     ...
;             PG8_LDB(B0, 0, 0); PG8_LDB(B1, 0, 1); PG8_SCHED; PG8_LDA(At, 0, 0); PG8_STAGE_A(PG8_SA(1, 1), vc10, vc11, kb1);
;             PG8_WAIT_V(12); PG8_WAIT_L(0); PG8_BAR; PG8_MMA(0, 0, At, B0); PG8_MMA(0, 1, At, B1); PG8_BAR; PG8_SCHED;
;             if (last) { vc10 = vn10; vc11 = vn11; }
;             PG8_BWAIT(2); PG8_BCOMMIT(0); PG8_SCHED; PG8_LDA(At, 0, 1); PG8_BISSUE(t + 3 >= nt ? pbn + (size_t)(t + 3 - nt) * 64 * Sched::LDN : pbc + (size_t)(t + 3) * 64 * Sched::LDN); PG8_STAGE_A(PG8_SA(0, 0), vc00, vc01, kb2);
;             PG8_WAIT_V(12); PG8_WAIT_L(0); PG8_BAR; if (half1) { PG8_MMA(1, 0, At, B0); PG8_MMA(1, 1, At, B1); } PG8_BAR; PG8_SCHED;
.LBB0_2448:
	v_add_u32_e32 v162, 0x10000, v247
	v_add_u32_e32 v174, 0x14000, v247
	ds_read_b128 v[178:181], v162
	ds_read_b128 v[182:185], v162 offset:1024
	ds_read_b128 v[186:189], v162 offset:2048
	ds_read_b128 v[190:193], v162 offset:3072
	ds_read_b128 v[162:165], v174
	ds_read_b128 v[166:169], v174 offset:1024
	ds_read_b128 v[170:173], v174 offset:2048
	ds_read_b128 v[174:177], v174 offset:3072
	s_lshl_b32 s5, s50, 7
	s_add_i32 s4, s5, 0x100
	v_cndmask_b32_e64 v228, v228, v250, s[28:29]
	v_readlane_b32 s54, v254, 53
	v_readlane_b32 s55, v254, 54
	s_add_u32 s30, s54, s5
	s_addc_u32 s31, s55, 0
	v_lshl_add_u64 v[236:237], s[30:31], 0, v[230:231]
	v_lshl_add_u64 v[236:237], v[236:237], 0, s[16:17]
	s_add_i32 m0, s35, 0xc000
	v_mov_b32_e32 v233, v231
	s_waitcnt lgkmcnt(0)
	ds_read_b128 v[194:197], v248
	ds_read_b128 v[198:201], v248 offset:1024
	ds_read_b128 v[202:205], v248 offset:2048
	ds_read_b128 v[206:209], v248 offset:3072
	ds_read_b128 v[210:213], v248 offset:4096
	ds_read_b128 v[214:217], v248 offset:5120
	ds_read_b128 v[218:221], v248 offset:6144
	ds_read_b128 v[222:225], v248 offset:7168
	global_load_lds_dwordx4 v[236:237], off
	v_lshl_add_u64 v[236:237], s[30:31], 0, v[232:233]
	v_lshl_add_u64 v[236:237], v[236:237], 0, s[16:17]
	s_add_i32 m0, s35, 0xe000
	s_nop 0
	global_load_lds_dwordx4 v[236:237], off
	s_waitcnt vmcnt(12)
	s_waitcnt lgkmcnt(0)
	s_barrier
	s_setprio 1
	s_waitcnt lgkmcnt(0)
	v_mfma_f32_16x16x32_bf16 v[158:161], v[178:181], v[194:197], v[158:161]
	v_mfma_f32_16x16x32_bf16 v[154:157], v[186:189], v[194:197], v[154:157]
	v_mfma_f32_16x16x32_bf16 v[142:145], v[178:181], v[202:205], v[142:145]
	v_mfma_f32_16x16x32_bf16 v[138:141], v[186:189], v[202:205], v[138:141]
	v_mfma_f32_16x16x32_bf16 v[126:129], v[178:181], v[210:213], v[126:129]
	v_mfma_f32_16x16x32_bf16 v[122:125], v[186:189], v[210:213], v[122:125]
	v_mfma_f32_16x16x32_bf16 v[110:113], v[178:181], v[218:221], v[110:113]
	v_mfma_f32_16x16x32_bf16 v[106:109], v[186:189], v[218:221], v[106:109]
	v_mfma_f32_16x16x32_bf16 v[158:161], v[182:185], v[198:201], v[158:161]
	v_mfma_f32_16x16x32_bf16 v[154:157], v[190:193], v[198:201], v[154:157]
	v_mfma_f32_16x16x32_bf16 v[142:145], v[182:185], v[206:209], v[142:145]
	v_mfma_f32_16x16x32_bf16 v[138:141], v[190:193], v[206:209], v[138:141]
	v_mfma_f32_16x16x32_bf16 v[126:129], v[182:185], v[214:217], v[126:129]
	v_mfma_f32_16x16x32_bf16 v[122:125], v[190:193], v[214:217], v[122:125]
	v_mfma_f32_16x16x32_bf16 v[110:113], v[182:185], v[222:225], v[110:113]
	v_mfma_f32_16x16x32_bf16 v[106:109], v[190:193], v[222:225], v[106:109]
	s_setprio 0
	s_setprio 1
	v_mfma_f32_16x16x32_bf16 v[150:153], v[162:165], v[194:197], v[150:153]
	v_mfma_f32_16x16x32_bf16 v[146:149], v[170:173], v[194:197], v[146:149]
	v_mfma_f32_16x16x32_bf16 v[134:137], v[162:165], v[202:205], v[134:137]
	v_mfma_f32_16x16x32_bf16 v[130:133], v[170:173], v[202:205], v[130:133]
	v_mfma_f32_16x16x32_bf16 v[118:121], v[162:165], v[210:213], v[118:121]
	v_mfma_f32_16x16x32_bf16 v[114:117], v[170:173], v[210:213], v[114:117]
	v_mfma_f32_16x16x32_bf16 v[102:105], v[162:165], v[218:221], v[102:105]
	v_mfma_f32_16x16x32_bf16 v[98:101], v[170:173], v[218:221], v[98:101]
	v_mfma_f32_16x16x32_bf16 v[150:153], v[166:169], v[198:201], v[150:153]
	v_mfma_f32_16x16x32_bf16 v[146:149], v[174:177], v[198:201], v[146:149]
	v_mfma_f32_16x16x32_bf16 v[134:137], v[166:169], v[206:209], v[134:137]
	v_mfma_f32_16x16x32_bf16 v[130:133], v[174:177], v[206:209], v[130:133]
	v_mfma_f32_16x16x32_bf16 v[118:121], v[166:169], v[214:217], v[118:121]
	v_mfma_f32_16x16x32_bf16 v[114:117], v[174:177], v[214:217], v[114:117]
	v_mfma_f32_16x16x32_bf16 v[102:105], v[166:169], v[222:225], v[102:105]
	v_mfma_f32_16x16x32_bf16 v[98:101], v[174:177], v[222:225], v[98:101]
	s_setprio 0
	s_barrier
	s_waitcnt vmcnt(2)
	v_cndmask_b32_e64 v226, v226, v249, s[28:29]
	v_add_u32_e32 v210, 0x10000, v242
	v_cvt_pk_bf16_f32 v194, v2, v6
	v_cvt_pk_bf16_f32 v195, v10, v14
	v_cvt_pk_bf16_f32 v196, v18, v22
	v_cvt_pk_bf16_f32 v197, v26, v30
	v_cvt_pk_bf16_f32 v198, v3, v7
	v_cvt_pk_bf16_f32 v199, v11, v15
	v_cvt_pk_bf16_f32 v200, v19, v23
	v_cvt_pk_bf16_f32 v201, v27, v31
	v_cvt_pk_bf16_f32 v202, v4, v8
	v_cvt_pk_bf16_f32 v203, v12, v16
	v_cvt_pk_bf16_f32 v204, v20, v24
	v_cvt_pk_bf16_f32 v205, v28, v32
	v_cvt_pk_bf16_f32 v206, v5, v9
	v_cvt_pk_bf16_f32 v207, v13, v17
	v_cvt_pk_bf16_f32 v208, v21, v25
	v_cvt_pk_bf16_f32 v209, v29, v33
	v_xor_b32_e32 v211, 64, v210
	v_xor_b32_e32 v212, 0x80, v210
	v_xor_b32_e32 v213, 0xc0, v210
	s_add_i32 s10, s50, -1
	s_lshl_b64 s[30:31], s[10:11], 18
	s_add_u32 s5, s47, s30
	s_addc_u32 s10, s21, s31
	s_and_b64 s[30:31], s[26:27], exec
	s_cselect_b32 s30, s48, s5
	s_cselect_b32 s31, s49, s10
	s_add_u32 s52, s30, 0x1000
	global_load_dwordx4 v[2:5], v240, s[30:31] offset:0
	s_addc_u32 s53, s31, 0
	global_load_dwordx4 v[6:9], v240, s[52:53] offset:0
	s_add_u32 s52, s30, 0x2000
	s_addc_u32 s53, s31, 0
	global_load_dwordx4 v[10:13], v240, s[52:53] offset:0
	s_add_u32 s52, s30, 0x3000
	s_addc_u32 s53, s31, 0
	global_load_dwordx4 v[14:17], v240, s[52:53] offset:0
	s_add_u32 s52, s30, 0x4000
	s_addc_u32 s53, s31, 0
	global_load_dwordx4 v[18:21], v240, s[52:53] offset:0
	s_add_u32 s52, s30, 0x5000
	s_addc_u32 s53, s31, 0
	global_load_dwordx4 v[22:25], v240, s[52:53] offset:0
	s_add_u32 s52, s30, 0x6000
	s_addc_u32 s53, s31, 0
	s_add_u32 s30, s30, 0x7000
	global_load_dwordx4 v[26:29], v240, s[52:53] offset:0
	s_addc_u32 s31, s31, 0
	global_load_dwordx4 v[30:33], v240, s[30:31] offset:0
	ds_write_b128 v210, v[194:197]
	ds_write_b128 v211, v[198:201]
	ds_write_b128 v212, v[202:205]
	ds_write_b128 v213, v[206:209]
	ds_read_b128 v[218:221], v248 offset:16384
	ds_read_b128 v[222:225], v248 offset:17408
	ds_read_b128 v[210:213], v248 offset:18432
	ds_read_b128 v[214:217], v248 offset:19456
	ds_read_b128 v[202:205], v248 offset:20480
	ds_read_b128 v[206:209], v248 offset:21504
	ds_read_b128 v[194:197], v248 offset:22528
	ds_read_b128 v[198:201], v248 offset:23552
	s_and_b64 s[30:31], s[28:29], exec
	s_cselect_b32 s4, 0, s4
	s_cselect_b32 s5, 0, 0
	s_add_u32 s30, s54, s4
	s_mov_b32 m0, s35
	s_addc_u32 s31, s55, s5
	global_load_lds_dwordx4 v226, s[30:31]
	s_mov_b32 m0, s36
	v_mov_b32_e32 v227, v231
	global_load_lds_dwordx4 v228, s[30:31]
	s_waitcnt vmcnt(12)
	s_waitcnt lgkmcnt(0)
	v_lshl_add_u64 v[238:239], s[30:31], 0, v[226:227]
	v_mov_b32_e32 v229, v231
	v_cndmask_b32_e64 v227, 0, 1, s[24:25]
	v_lshl_add_u64 v[236:237], s[30:31], 0, v[228:229]
	v_cmp_ne_u32_e64 s[4:5], 1, v227
	s_andn2_b64 vcc, exec, s[24:25]
	s_barrier
; #define PG8_STAGE_A(bufoff, V0, V1, kb) do { \
;         __builtin_amdgcn_global_load_lds((const unsigned*)((Abase + (kb)) + (V0)), (LAS unsigned*)(lds + (bufoff) + ldsw), 16, 0, 0); \
;         __builtin_amdgcn_global_load_lds((const unsigned*)((Abase + (kb)) + (V1)), (LAS unsigned*)(lds + (bufoff) + ldsw + 8192), 16, 0, 0); } while (0)
; #define PG8_LDA(dst, b, h) do { _Pragma("unroll") for (int m = 0; m < 4; ++m) _Pragma("unroll") for (int k = 0; k < 2; ++k) dst[m][k] = *(const LAS bf16x8*)(lds + PG8_SA(b, h) + aoff + m * 2048 + k * 1024); } while (0)
; #define PG8_LDB(dst, b, h) do { _Pragma("unroll") for (int n = 0; n < 2; ++n) _Pragma("unroll") for (int k = 0; k < 2; ++k) dst[n][k] = *(const LAS bf16x8*)(lds + PG8_SB(b, h) + boff + n * 2048 + k * 1024); } while (0)
; #define PG8_MMA(ai, bj, At, Bt) do { __builtin_amdgcn_s_setprio(1); _Pragma("unroll") for (int m = 0; m < 4; ++m) _Pragma("unroll") for (int n = 0; n < 2; ++n) _Pragma("unroll") for (int k = 0; k < 2; ++k) \
;         acc[ai][bj][m][n] = __builtin_amdgcn_mfma_f32_16x16x32_bf16(Bt[n][k], At[m][k], acc[ai][bj][m][n], 0, 0, 0); __builtin_amdgcn_s_setprio(0); } while (0)
; #define PG8_WAIT_V(n) asm volatile("s_waitcnt vmcnt(" #n ")" ::: "memory")
; #define PG8_WAIT_L(n) asm volatile("s_waitcnt lgkmcnt(" #n ")" ::: "memory")
; #define PG8_BAR __builtin_amdgcn_s_barrier()
; #define PG8_SCHED __builtin_amdgcn_sched_barrier(0)
; template <class Epi, class Sched, bool ALIGN_EPI>
; __device__ __forceinline__ void gemm_phase(LAS unsigned char* lds, const Gemm g, const Sched& S, const Epi& E) {
;     ...
;             PG8_WAIT_V(12); PG8_WAIT_L(0); PG8_BAR; if (half1) { PG8_MMA(1, 0, At, B0); PG8_MMA(1, 1, At, B1); } PG8_BAR; PG8_SCHED;
;             PG8_LDB(B0, 1, 0); PG8_LDB(B1, 1, 1); PG8_SCHED; PG8_LDA(At, 1, 0); PG8_STAGE_A(PG8_SA(0, 1), vc10, vc11, kb2);
;             PG8_WAIT_V(12); PG8_WAIT_L(0); PG8_BAR; PG8_MMA(0, 0, At, B0); PG8_MMA(0, 1, At, B1); PG8_BAR; PG8_SCHED;
	s_cbranch_vccnz .LBB0_2450
	s_setprio 1
	s_waitcnt lgkmcnt(0)
	v_mfma_f32_16x16x32_bf16 v[94:97], v[178:181], v[218:221], v[94:97]
	v_mfma_f32_16x16x32_bf16 v[90:93], v[186:189], v[218:221], v[90:93]
	v_mfma_f32_16x16x32_bf16 v[78:81], v[178:181], v[210:213], v[78:81]
	v_mfma_f32_16x16x32_bf16 v[74:77], v[186:189], v[210:213], v[74:77]
	v_mfma_f32_16x16x32_bf16 v[62:65], v[178:181], v[202:205], v[62:65]
	v_mfma_f32_16x16x32_bf16 v[58:61], v[186:189], v[202:205], v[58:61]
	v_mfma_f32_16x16x32_bf16 v[46:49], v[178:181], v[194:197], v[46:49]
	v_mfma_f32_16x16x32_bf16 v[42:45], v[186:189], v[194:197], v[42:45]
	v_mfma_f32_16x16x32_bf16 v[94:97], v[182:185], v[222:225], v[94:97]
	v_mfma_f32_16x16x32_bf16 v[90:93], v[190:193], v[222:225], v[90:93]
	v_mfma_f32_16x16x32_bf16 v[78:81], v[182:185], v[214:217], v[78:81]
	v_mfma_f32_16x16x32_bf16 v[74:77], v[190:193], v[214:217], v[74:77]
	v_mfma_f32_16x16x32_bf16 v[62:65], v[182:185], v[206:209], v[62:65]
	v_mfma_f32_16x16x32_bf16 v[58:61], v[190:193], v[206:209], v[58:61]
	v_mfma_f32_16x16x32_bf16 v[46:49], v[182:185], v[198:201], v[46:49]
	v_mfma_f32_16x16x32_bf16 v[42:45], v[190:193], v[198:201], v[42:45]
	s_setprio 0
	s_setprio 1
	v_mfma_f32_16x16x32_bf16 v[86:89], v[162:165], v[218:221], v[86:89]
	v_mfma_f32_16x16x32_bf16 v[82:85], v[170:173], v[218:221], v[82:85]
	v_mfma_f32_16x16x32_bf16 v[70:73], v[162:165], v[210:213], v[70:73]
	v_mfma_f32_16x16x32_bf16 v[66:69], v[170:173], v[210:213], v[66:69]
	v_mfma_f32_16x16x32_bf16 v[54:57], v[162:165], v[202:205], v[54:57]
	v_mfma_f32_16x16x32_bf16 v[50:53], v[170:173], v[202:205], v[50:53]
	v_mfma_f32_16x16x32_bf16 v[38:41], v[162:165], v[194:197], v[38:41]
	v_mfma_f32_16x16x32_bf16 v[34:37], v[170:173], v[194:197], v[34:37]
	v_mfma_f32_16x16x32_bf16 v[86:89], v[166:169], v[222:225], v[86:89]
	v_mfma_f32_16x16x32_bf16 v[82:85], v[174:177], v[222:225], v[82:85]
	v_mfma_f32_16x16x32_bf16 v[70:73], v[166:169], v[214:217], v[70:73]
	v_mfma_f32_16x16x32_bf16 v[66:69], v[174:177], v[214:217], v[66:69]
	v_mfma_f32_16x16x32_bf16 v[54:57], v[166:169], v[206:209], v[54:57]
	v_mfma_f32_16x16x32_bf16 v[50:53], v[174:177], v[206:209], v[50:53]
	v_mfma_f32_16x16x32_bf16 v[38:41], v[166:169], v[198:201], v[38:41]
	v_mfma_f32_16x16x32_bf16 v[34:37], v[174:177], v[198:201], v[34:37]
	s_setprio 0
.LBB0_2450:
	v_cndmask_b32_e64 v232, v232, v252, s[28:29]
	v_cndmask_b32_e64 v230, v230, v251, s[28:29]
	s_barrier
	v_add_u32_e32 v162, 0x18000, v247
	v_add_u32_e32 v174, 0x1c000, v247
	ds_read_b128 v[178:181], v162
	ds_read_b128 v[182:185], v162 offset:1024
	ds_read_b128 v[186:189], v162 offset:2048
	ds_read_b128 v[190:193], v162 offset:3072
	ds_read_b128 v[162:165], v174
	ds_read_b128 v[166:169], v174 offset:1024
	ds_read_b128 v[170:173], v174 offset:2048
	ds_read_b128 v[174:177], v174 offset:3072
	s_mov_b32 m0, s37
	s_waitcnt lgkmcnt(0)
	ds_read_b128 v[194:197], v248 offset:32768
	ds_read_b128 v[198:201], v248 offset:33792
	ds_read_b128 v[202:205], v248 offset:34816
	ds_read_b128 v[206:209], v248 offset:35840
	ds_read_b128 v[210:213], v248 offset:36864
	ds_read_b128 v[214:217], v248 offset:37888
	ds_read_b128 v[218:221], v248 offset:38912
	ds_read_b128 v[222:225], v248 offset:39936
	global_load_lds_dwordx4 v230, s[30:31]
	s_mov_b32 m0, s38
	s_nop 0
	global_load_lds_dwordx4 v232, s[30:31]
	s_waitcnt vmcnt(12)
	s_waitcnt lgkmcnt(0)
	s_barrier
	s_setprio 1
	s_waitcnt lgkmcnt(0)
	v_mfma_f32_16x16x32_bf16 v[158:161], v[178:181], v[194:197], v[158:161]
	v_mfma_f32_16x16x32_bf16 v[154:157], v[186:189], v[194:197], v[154:157]
	v_mfma_f32_16x16x32_bf16 v[142:145], v[178:181], v[202:205], v[142:145]
	v_mfma_f32_16x16x32_bf16 v[138:141], v[186:189], v[202:205], v[138:141]
	v_mfma_f32_16x16x32_bf16 v[126:129], v[178:181], v[210:213], v[126:129]
	v_mfma_f32_16x16x32_bf16 v[122:125], v[186:189], v[210:213], v[122:125]
	v_mfma_f32_16x16x32_bf16 v[110:113], v[178:181], v[218:221], v[110:113]
	v_mfma_f32_16x16x32_bf16 v[106:109], v[186:189], v[218:221], v[106:109]
	v_mfma_f32_16x16x32_bf16 v[158:161], v[182:185], v[198:201], v[158:161]
	v_mfma_f32_16x16x32_bf16 v[154:157], v[190:193], v[198:201], v[154:157]
	v_mfma_f32_16x16x32_bf16 v[142:145], v[182:185], v[206:209], v[142:145]
	v_mfma_f32_16x16x32_bf16 v[138:141], v[190:193], v[206:209], v[138:141]
	v_mfma_f32_16x16x32_bf16 v[126:129], v[182:185], v[214:217], v[126:129]
	v_mfma_f32_16x16x32_bf16 v[122:125], v[190:193], v[214:217], v[122:125]
	v_mfma_f32_16x16x32_bf16 v[110:113], v[182:185], v[222:225], v[110:113]
	v_mfma_f32_16x16x32_bf16 v[106:109], v[190:193], v[222:225], v[106:109]
	s_setprio 0
	s_setprio 1
	v_mfma_f32_16x16x32_bf16 v[150:153], v[162:165], v[194:197], v[150:153]
	v_mfma_f32_16x16x32_bf16 v[146:149], v[170:173], v[194:197], v[146:149]
	v_mfma_f32_16x16x32_bf16 v[134:137], v[162:165], v[202:205], v[134:137]
	v_mfma_f32_16x16x32_bf16 v[130:133], v[170:173], v[202:205], v[130:133]
	v_mfma_f32_16x16x32_bf16 v[118:121], v[162:165], v[210:213], v[118:121]
	v_mfma_f32_16x16x32_bf16 v[114:117], v[170:173], v[210:213], v[114:117]
	v_mfma_f32_16x16x32_bf16 v[102:105], v[162:165], v[218:221], v[102:105]
	v_mfma_f32_16x16x32_bf16 v[98:101], v[170:173], v[218:221], v[98:101]
	v_mfma_f32_16x16x32_bf16 v[150:153], v[166:169], v[198:201], v[150:153]
	v_mfma_f32_16x16x32_bf16 v[146:149], v[174:177], v[198:201], v[146:149]
	v_mfma_f32_16x16x32_bf16 v[134:137], v[166:169], v[206:209], v[134:137]
	v_mfma_f32_16x16x32_bf16 v[130:133], v[174:177], v[206:209], v[130:133]
	v_mfma_f32_16x16x32_bf16 v[118:121], v[166:169], v[214:217], v[118:121]
	v_mfma_f32_16x16x32_bf16 v[114:117], v[174:177], v[214:217], v[114:117]
	v_mfma_f32_16x16x32_bf16 v[102:105], v[166:169], v[222:225], v[102:105]
	v_mfma_f32_16x16x32_bf16 v[98:101], v[174:177], v[222:225], v[98:101]
	s_setprio 0
	s_barrier
; #define PG8_BWAIT(n) asm volatile("s_waitcnt vmcnt(" #n ")" : "+v"(bv[0]), "+v"(bv[1]), "+v"(bv[2]), "+v"(bv[3]), "+v"(bv[4]), "+v"(bv[5]), "+v"(bv[6]), "+v"(bv[7]) :: "memory")
; #define PG8_STAGE_A(bufoff, V0, V1, kb) do { \
;         __builtin_amdgcn_global_load_lds((const unsigned*)((Abase + (kb)) + (V0)), (LAS unsigned*)(lds + (bufoff) + ldsw), 16, 0, 0); \
;         __builtin_amdgcn_global_load_lds((const unsigned*)((Abase + (kb)) + (V1)), (LAS unsigned*)(lds + (bufoff) + ldsw + 8192), 16, 0, 0); } while (0)
; #define PG8_LDA(dst, b, h) do { _Pragma("unroll") for (int m = 0; m < 4; ++m) _Pragma("unroll") for (int k = 0; k < 2; ++k) dst[m][k] = *(const LAS bf16x8*)(lds + PG8_SA(b, h) + aoff + m * 2048 + k * 1024); } while (0)
; #define PG8_MMA(ai, bj, At, Bt) do { __builtin_amdgcn_s_setprio(1); _Pragma("unroll") for (int m = 0; m < 4; ++m) _Pragma("unroll") for (int n = 0; n < 2; ++n) _Pragma("unroll") for (int k = 0; k < 2; ++k) \
;         acc[ai][bj][m][n] = __builtin_amdgcn_mfma_f32_16x16x32_bf16(Bt[n][k], At[m][k], acc[ai][bj][m][n], 0, 0, 0); __builtin_amdgcn_s_setprio(0); } while (0)
; #define PG8_WAIT_V(n) asm volatile("s_waitcnt vmcnt(" #n ")" ::: "memory")
; #define PG8_WAIT_L(n) asm volatile("s_waitcnt lgkmcnt(" #n ")" ::: "memory")
; #define PG8_BAR __builtin_amdgcn_s_barrier()
; #define PG8_SCHED __builtin_amdgcn_sched_barrier(0)
; template <class Epi, class Sched, bool ALIGN_EPI>
; __device__ __forceinline__ void gemm_phase(LAS unsigned char* lds, const Gemm g, const Sched& S, const Epi& E) {
;     ...
;             PG8_BWAIT(2); PG8_BCOMMIT(1); PG8_SCHED; PG8_LDA(At, 1, 1); PG8_BISSUE(t + 4 >= nt ? pbn + (size_t)(t + 4 - nt) * 64 * Sched::LDN : pbc + (size_t)(t + 4) * 64 * Sched::LDN); PG8_STAGE_A(PG8_SA(1, 0), vc00, vc01, kb2 + 128u);
;             PG8_WAIT_V(12); PG8_WAIT_L(0); PG8_BAR; if (half1) { PG8_MMA(1, 0, At, B0); PG8_MMA(1, 1, At, B1); } PG8_BAR; PG8_SCHED;
	s_waitcnt vmcnt(2)
	s_nop 0
	v_add_u32_e32 v210, 0x18000, v242
	v_cvt_pk_bf16_f32 v194, v2, v6
	v_cvt_pk_bf16_f32 v195, v10, v14
	v_cvt_pk_bf16_f32 v196, v18, v22
	v_cvt_pk_bf16_f32 v197, v26, v30
	v_cvt_pk_bf16_f32 v198, v3, v7
	v_cvt_pk_bf16_f32 v199, v11, v15
	v_cvt_pk_bf16_f32 v200, v19, v23
	v_cvt_pk_bf16_f32 v201, v27, v31
	v_cvt_pk_bf16_f32 v202, v4, v8
	v_cvt_pk_bf16_f32 v203, v12, v16
	v_cvt_pk_bf16_f32 v204, v20, v24
	v_cvt_pk_bf16_f32 v205, v28, v32
	v_cvt_pk_bf16_f32 v206, v5, v9
	v_cvt_pk_bf16_f32 v207, v13, v17
	v_cvt_pk_bf16_f32 v208, v21, v25
	v_cvt_pk_bf16_f32 v209, v29, v33
	v_xor_b32_e32 v211, 64, v210
	v_xor_b32_e32 v212, 0x80, v210
	v_xor_b32_e32 v213, 0xc0, v210
	s_lshl_b32 s10, s50, 16
	s_lshl_b64 s[28:29], s[10:11], 2
	s_add_u32 s28, s47, s28
	s_addc_u32 s29, s21, s29
	s_add_u32 s30, s28, 0x1000
	global_load_dwordx4 v[2:5], v240, s[28:29] offset:0
	s_addc_u32 s31, s29, 0
	global_load_dwordx4 v[6:9], v240, s[30:31] offset:0
	s_add_u32 s30, s28, 0x2000
	s_addc_u32 s31, s29, 0
	global_load_dwordx4 v[10:13], v240, s[30:31] offset:0
	s_add_u32 s30, s28, 0x3000
	s_addc_u32 s31, s29, 0
	global_load_dwordx4 v[14:17], v240, s[30:31] offset:0
	s_add_u32 s30, s28, 0x4000
	s_addc_u32 s31, s29, 0
	global_load_dwordx4 v[18:21], v240, s[30:31] offset:0
	s_add_u32 s30, s28, 0x5000
	s_addc_u32 s31, s29, 0
	global_load_dwordx4 v[22:25], v240, s[30:31] offset:0
	s_add_u32 s30, s28, 0x6000
	s_addc_u32 s31, s29, 0
	global_load_dwordx4 v[26:29], v240, s[30:31] offset:0
	s_add_u32 s28, s28, 0x7000
	s_mov_b32 m0, s39
	s_addc_u32 s29, s29, 0
	global_load_dwordx4 v[30:33], v240, s[28:29] offset:0
	ds_write_b128 v210, v[194:197]
	ds_write_b128 v211, v[198:201]
	ds_write_b128 v212, v[202:205]
	ds_write_b128 v213, v[206:209]
	ds_read_b128 v[218:221], v248 offset:49152
	ds_read_b128 v[222:225], v248 offset:50176
	ds_read_b128 v[210:213], v248 offset:51200
	ds_read_b128 v[214:217], v248 offset:52224
	ds_read_b128 v[202:205], v248 offset:53248
	ds_read_b128 v[206:209], v248 offset:54272
	ds_read_b128 v[194:197], v248 offset:55296
	ds_read_b128 v[198:201], v248 offset:56320
	v_lshl_add_u64 v[238:239], v[238:239], 0, s[16:17]
	global_load_lds_dwordx4 v[238:239], off
	v_lshl_add_u64 v[236:237], v[236:237], 0, s[16:17]
	s_mov_b32 m0, s40
	s_and_b64 vcc, exec, s[4:5]
	global_load_lds_dwordx4 v[236:237], off
	s_waitcnt vmcnt(12)
	s_waitcnt lgkmcnt(0)
	s_barrier
	s_cbranch_vccnz .LBB0_2447
	s_setprio 1
	s_waitcnt lgkmcnt(0)
	v_mfma_f32_16x16x32_bf16 v[94:97], v[178:181], v[218:221], v[94:97]
	v_mfma_f32_16x16x32_bf16 v[90:93], v[186:189], v[218:221], v[90:93]
	v_mfma_f32_16x16x32_bf16 v[78:81], v[178:181], v[210:213], v[78:81]
	v_mfma_f32_16x16x32_bf16 v[74:77], v[186:189], v[210:213], v[74:77]
	v_mfma_f32_16x16x32_bf16 v[62:65], v[178:181], v[202:205], v[62:65]
	v_mfma_f32_16x16x32_bf16 v[58:61], v[186:189], v[202:205], v[58:61]
	v_mfma_f32_16x16x32_bf16 v[46:49], v[178:181], v[194:197], v[46:49]
	v_mfma_f32_16x16x32_bf16 v[42:45], v[186:189], v[194:197], v[42:45]
	v_mfma_f32_16x16x32_bf16 v[94:97], v[182:185], v[222:225], v[94:97]
	v_mfma_f32_16x16x32_bf16 v[90:93], v[190:193], v[222:225], v[90:93]
	v_mfma_f32_16x16x32_bf16 v[78:81], v[182:185], v[214:217], v[78:81]
	v_mfma_f32_16x16x32_bf16 v[74:77], v[190:193], v[214:217], v[74:77]
	v_mfma_f32_16x16x32_bf16 v[62:65], v[182:185], v[206:209], v[62:65]
	v_mfma_f32_16x16x32_bf16 v[58:61], v[190:193], v[206:209], v[58:61]
	v_mfma_f32_16x16x32_bf16 v[46:49], v[182:185], v[198:201], v[46:49]
	v_mfma_f32_16x16x32_bf16 v[42:45], v[190:193], v[198:201], v[42:45]
	s_setprio 0
	s_setprio 1
	v_mfma_f32_16x16x32_bf16 v[86:89], v[162:165], v[218:221], v[86:89]
	v_mfma_f32_16x16x32_bf16 v[82:85], v[170:173], v[218:221], v[82:85]
	v_mfma_f32_16x16x32_bf16 v[70:73], v[162:165], v[210:213], v[70:73]
	v_mfma_f32_16x16x32_bf16 v[66:69], v[170:173], v[210:213], v[66:69]
	v_mfma_f32_16x16x32_bf16 v[54:57], v[162:165], v[202:205], v[54:57]
	v_mfma_f32_16x16x32_bf16 v[50:53], v[170:173], v[202:205], v[50:53]
	v_mfma_f32_16x16x32_bf16 v[38:41], v[162:165], v[194:197], v[38:41]
	v_mfma_f32_16x16x32_bf16 v[34:37], v[170:173], v[194:197], v[34:37]
	v_mfma_f32_16x16x32_bf16 v[86:89], v[166:169], v[222:225], v[86:89]
	v_mfma_f32_16x16x32_bf16 v[82:85], v[174:177], v[222:225], v[82:85]
	v_mfma_f32_16x16x32_bf16 v[70:73], v[166:169], v[214:217], v[70:73]
	v_mfma_f32_16x16x32_bf16 v[66:69], v[174:177], v[214:217], v[66:69]
	v_mfma_f32_16x16x32_bf16 v[54:57], v[166:169], v[206:209], v[54:57]
	v_mfma_f32_16x16x32_bf16 v[50:53], v[174:177], v[206:209], v[50:53]
	v_mfma_f32_16x16x32_bf16 v[38:41], v[166:169], v[198:201], v[38:41]
	v_mfma_f32_16x16x32_bf16 v[34:37], v[174:177], v[198:201], v[34:37]
	s_setprio 0
	s_branch .LBB0_2447

; #define PG8_BWAIT(n) asm volatile("s_waitcnt vmcnt(" #n ")" : "+v"(bv[0]), "+v"(bv[1]), "+v"(bv[2]), "+v"(bv[3]), "+v"(bv[4]), "+v"(bv[5]), "+v"(bv[6]), "+v"(bv[7]) :: "memory")
; #define PG8_STAGE_A(bufoff, V0, V1, kb) do { \
;         __builtin_amdgcn_global_load_lds((const unsigned*)((Abase + (kb)) + (V0)), (LAS unsigned*)(lds + (bufoff) + ldsw), 16, 0, 0); \
;         __builtin_amdgcn_global_load_lds((const unsigned*)((Abase + (kb)) + (V1)), (LAS unsigned*)(lds + (bufoff) + ldsw + 8192), 16, 0, 0); } while (0)
; #define PG8_LDA(dst, b, h) do { _Pragma("unroll") for (int m = 0; m < 4; ++m) _Pragma("unroll") for (int k = 0; k < 2; ++k) dst[m][k] = *(const LAS bf16x8*)(lds + PG8_SA(b, h) + aoff + m * 2048 + k * 1024); } while (0)
; #define PG8_LDB(dst, b, h) do { _Pragma("unroll") for (int n = 0; n < 2; ++n) _Pragma("unroll") for (int k = 0; k < 2; ++k) dst[n][k] = *(const LAS bf16x8*)(lds + PG8_SB(b, h) + boff + n * 2048 + k * 1024); } while (0)
; #define PG8_MMA(ai, bj, At, Bt) do { __builtin_amdgcn_s_setprio(1); _Pragma("unroll") for (int m = 0; m < 4; ++m) _Pragma("unroll") for (int n = 0; n < 2; ++n) _Pragma("unroll") for (int k = 0; k < 2; ++k) \
;         acc[ai][bj][m][n] = __builtin_amdgcn_mfma_f32_16x16x32_bf16(Bt[n][k], At[m][k], acc[ai][bj][m][n], 0, 0, 0); __builtin_amdgcn_s_setprio(0); } while (0)
; #define PG8_WAIT_V(n) asm volatile("s_waitcnt vmcnt(" #n ")" ::: "memory")
; #define PG8_WAIT_L(n) asm volatile("s_waitcnt lgkmcnt(" #n ")" ::: "memory")
; #define PG8_BAR __builtin_amdgcn_s_barrier()
; #define PG8_SCHED __builtin_amdgcn_sched_barrier(0)
; template <class Epi, class Sched, bool ALIGN_EPI>
; __device__ __forceinline__ void gemm_phase(LAS unsigned char* lds, const Gemm g, const Sched& S, const Epi& E) {
;     ...
;             PG8_LDB(B0, 0, 0); PG8_LDB(B1, 0, 1); PG8_SCHED; PG8_LDA(At, 0, 0); PG8_STAGE_A(PG8_SA(1, 1), vc10, vc11, kb1);
;             PG8_WAIT_V(12); PG8_WAIT_L(0); PG8_BAR; PG8_MMA(0, 0, At, B0); PG8_MMA(0, 1, At, B1); PG8_BAR; PG8_SCHED;
;             if (last) { vc10 = vn10; vc11 = vn11; }
;             PG8_BWAIT(2); PG8_BCOMMIT(0); PG8_SCHED; PG8_LDA(At, 0, 1); PG8_BISSUE(t + 3 >= nt ? pbn + (size_t)(t + 3 - nt) * 64 * Sched::LDN : pbc + (size_t)(t + 3) * 64 * Sched::LDN); PG8_STAGE_A(PG8_SA(0, 0), vc00, vc01, kb2);
.LBB0_4711:
	v_add_u32_e32 v162, 0x10000, v240
	v_add_u32_e32 v174, 0x14000, v240
	ds_read_b128 v[178:181], v162
	ds_read_b128 v[182:185], v162 offset:1024
	ds_read_b128 v[186:189], v162 offset:2048
	ds_read_b128 v[190:193], v162 offset:3072
	ds_read_b128 v[162:165], v174
	ds_read_b128 v[166:169], v174 offset:1024
	ds_read_b128 v[170:173], v174 offset:2048
	ds_read_b128 v[174:177], v174 offset:3072
	s_add_i32 s54, s53, 2
	s_add_i32 m0, s40, 0xc000
	s_add_u32 s2, s90, s22
	s_addc_u32 s3, s91, s23
	s_waitcnt lgkmcnt(0)
	ds_read_b128 v[194:197], v241
	ds_read_b128 v[198:201], v241 offset:1024
	ds_read_b128 v[202:205], v241 offset:2048
	ds_read_b128 v[206:209], v241 offset:3072
	ds_read_b128 v[210:213], v241 offset:4096
	ds_read_b128 v[214:217], v241 offset:5120
	ds_read_b128 v[218:221], v241 offset:6144
	ds_read_b128 v[222:225], v241 offset:7168
	global_load_lds_dwordx4 v233, s[2:3]
	s_add_i32 m0, s40, 0xe000
	s_nop 0
	global_load_lds_dwordx4 v234, s[2:3]
	s_waitcnt vmcnt(12)
	s_waitcnt lgkmcnt(0)
	s_barrier
	s_setprio 1
	s_waitcnt lgkmcnt(0)
	v_mfma_f32_16x16x32_bf16 v[158:161], v[178:181], v[194:197], v[158:161]
	v_mfma_f32_16x16x32_bf16 v[154:157], v[186:189], v[194:197], v[154:157]
	v_mfma_f32_16x16x32_bf16 v[142:145], v[178:181], v[202:205], v[142:145]
	v_mfma_f32_16x16x32_bf16 v[138:141], v[186:189], v[202:205], v[138:141]
	v_mfma_f32_16x16x32_bf16 v[126:129], v[178:181], v[210:213], v[126:129]
	v_mfma_f32_16x16x32_bf16 v[122:125], v[186:189], v[210:213], v[122:125]
	v_mfma_f32_16x16x32_bf16 v[110:113], v[178:181], v[218:221], v[110:113]
	v_mfma_f32_16x16x32_bf16 v[106:109], v[186:189], v[218:221], v[106:109]
	v_mfma_f32_16x16x32_bf16 v[158:161], v[182:185], v[198:201], v[158:161]
	v_mfma_f32_16x16x32_bf16 v[154:157], v[190:193], v[198:201], v[154:157]
	v_mfma_f32_16x16x32_bf16 v[142:145], v[182:185], v[206:209], v[142:145]
	v_mfma_f32_16x16x32_bf16 v[138:141], v[190:193], v[206:209], v[138:141]
	v_mfma_f32_16x16x32_bf16 v[126:129], v[182:185], v[214:217], v[126:129]
	v_mfma_f32_16x16x32_bf16 v[122:125], v[190:193], v[214:217], v[122:125]
	v_mfma_f32_16x16x32_bf16 v[110:113], v[182:185], v[222:225], v[110:113]
	v_mfma_f32_16x16x32_bf16 v[106:109], v[190:193], v[222:225], v[106:109]
	s_setprio 0
	s_setprio 1
	v_mfma_f32_16x16x32_bf16 v[150:153], v[162:165], v[194:197], v[150:153]
	v_mfma_f32_16x16x32_bf16 v[146:149], v[170:173], v[194:197], v[146:149]
	v_mfma_f32_16x16x32_bf16 v[134:137], v[162:165], v[202:205], v[134:137]
	v_mfma_f32_16x16x32_bf16 v[130:133], v[170:173], v[202:205], v[130:133]
	v_mfma_f32_16x16x32_bf16 v[118:121], v[162:165], v[210:213], v[118:121]
	v_mfma_f32_16x16x32_bf16 v[114:117], v[170:173], v[210:213], v[114:117]
	v_mfma_f32_16x16x32_bf16 v[102:105], v[162:165], v[218:221], v[102:105]
	v_mfma_f32_16x16x32_bf16 v[98:101], v[170:173], v[218:221], v[98:101]
	v_mfma_f32_16x16x32_bf16 v[150:153], v[166:169], v[198:201], v[150:153]
	v_mfma_f32_16x16x32_bf16 v[146:149], v[174:177], v[198:201], v[146:149]
	v_mfma_f32_16x16x32_bf16 v[134:137], v[166:169], v[206:209], v[134:137]
	v_mfma_f32_16x16x32_bf16 v[130:133], v[174:177], v[206:209], v[130:133]
	v_mfma_f32_16x16x32_bf16 v[118:121], v[166:169], v[214:217], v[118:121]
	v_mfma_f32_16x16x32_bf16 v[114:117], v[174:177], v[214:217], v[114:117]
	v_mfma_f32_16x16x32_bf16 v[102:105], v[166:169], v[222:225], v[102:105]
	v_mfma_f32_16x16x32_bf16 v[98:101], v[174:177], v[222:225], v[98:101]
	s_setprio 0
	s_barrier
	s_waitcnt vmcnt(2)
	s_nop 0
	v_add_u32_e32 v210, 0x10000, v235
	v_cvt_pk_bf16_f32 v194, v2, v6
	v_cvt_pk_bf16_f32 v195, v10, v14
	v_cvt_pk_bf16_f32 v196, v18, v22
	v_cvt_pk_bf16_f32 v197, v26, v30
	v_cvt_pk_bf16_f32 v198, v3, v7
	v_cvt_pk_bf16_f32 v199, v11, v15
	v_cvt_pk_bf16_f32 v200, v19, v23
	v_cvt_pk_bf16_f32 v201, v27, v31
	v_cvt_pk_bf16_f32 v202, v4, v8
	v_cvt_pk_bf16_f32 v203, v12, v16
	v_cvt_pk_bf16_f32 v204, v20, v24
	v_cvt_pk_bf16_f32 v205, v28, v32
	v_cvt_pk_bf16_f32 v206, v5, v9
	v_cvt_pk_bf16_f32 v207, v13, v17
	v_cvt_pk_bf16_f32 v208, v21, v25
	v_cvt_pk_bf16_f32 v209, v29, v33
	v_xor_b32_e32 v211, 64, v210
	v_xor_b32_e32 v212, 0x80, v210
	v_xor_b32_e32 v213, 0xc0, v210
	s_cmp_lt_u32 s54, 13
	s_mov_b64 s[4:5], -1
	s_cbranch_scc0 .LBB0_4713
	s_add_u32 s2, s20, 0x30000
	s_addc_u32 s3, s21, 0
	s_mov_b64 s[4:5], 0

; #define PG8_BWAIT(n) asm volatile("s_waitcnt vmcnt(" #n ")" : "+v"(bv[0]), "+v"(bv[1]), "+v"(bv[2]), "+v"(bv[3]), "+v"(bv[4]), "+v"(bv[5]), "+v"(bv[6]), "+v"(bv[7]) :: "memory")
; #define PG8_STAGE_A(bufoff, V0, V1, kb) do { \
;         __builtin_amdgcn_global_load_lds((const unsigned*)((Abase + (kb)) + (V0)), (LAS unsigned*)(lds + (bufoff) + ldsw), 16, 0, 0); \
;         __builtin_amdgcn_global_load_lds((const unsigned*)((Abase + (kb)) + (V1)), (LAS unsigned*)(lds + (bufoff) + ldsw + 8192), 16, 0, 0); } while (0)
; #define PG8_LDA(dst, b, h) do { _Pragma("unroll") for (int m = 0; m < 4; ++m) _Pragma("unroll") for (int k = 0; k < 2; ++k) dst[m][k] = *(const LAS bf16x8*)(lds + PG8_SA(b, h) + aoff + m * 2048 + k * 1024); } while (0)
; #define PG8_MMA(ai, bj, At, Bt) do { __builtin_amdgcn_s_setprio(1); _Pragma("unroll") for (int m = 0; m < 4; ++m) _Pragma("unroll") for (int n = 0; n < 2; ++n) _Pragma("unroll") for (int k = 0; k < 2; ++k) \
;         acc[ai][bj][m][n] = __builtin_amdgcn_mfma_f32_16x16x32_bf16(Bt[n][k], At[m][k], acc[ai][bj][m][n], 0, 0, 0); __builtin_amdgcn_s_setprio(0); } while (0)
; #define PG8_WAIT_V(n) asm volatile("s_waitcnt vmcnt(" #n ")" ::: "memory")
; #define PG8_WAIT_L(n) asm volatile("s_waitcnt lgkmcnt(" #n ")" ::: "memory")
; #define PG8_BAR __builtin_amdgcn_s_barrier()
; #define PG8_SCHED __builtin_amdgcn_sched_barrier(0)
; template <class Epi, class Sched, bool ALIGN_EPI>
; __device__ __forceinline__ void gemm_phase(LAS unsigned char* lds, const Gemm g, const Sched& S, const Epi& E) {
;     ...
;             PG8_BWAIT(2); PG8_BCOMMIT(0); PG8_SCHED; PG8_LDA(At, 0, 1); PG8_BISSUE(t + 3 >= nt ? pbn + (size_t)(t + 3 - nt) * 64 * Sched::LDN : pbc + (size_t)(t + 3) * 64 * Sched::LDN); PG8_STAGE_A(PG8_SA(0, 0), vc00, vc01, kb2);
;             PG8_WAIT_V(12); PG8_WAIT_L(0); PG8_BAR; if (half1) { PG8_MMA(1, 0, At, B0); PG8_MMA(1, 1, At, B1); } PG8_BAR; PG8_SCHED;
.LBB0_4715:
	s_add_i32 s8, s22, 0xe8940080
	s_cmp_eq_u32 s53, 12
	global_load_dwordx4 v[2:5], v232, s[2:3] offset:0
	s_cselect_b64 s[4:5], -1, 0
	global_load_dwordx4 v[6:9], v232, s[2:3] offset:0x400
	s_and_b64 s[26:27], s[4:5], exec
	global_load_dwordx4 v[10:13], v232, s[2:3] offset:0x800
	s_cselect_b32 s8, 0, s8
	global_load_dwordx4 v[14:17], v232, s[2:3] offset:0xc00
	s_add_u32 s2, s2, 0x1000
	s_addc_u32 s3, s3, 0
	global_load_dwordx4 v[18:21], v232, s[2:3] offset:0
	global_load_dwordx4 v[22:25], v232, s[2:3] offset:0x400
	global_load_dwordx4 v[26:29], v232, s[2:3] offset:0x800
	global_load_dwordx4 v[30:33], v232, s[2:3] offset:0xc00
	ds_write_b128 v210, v[194:197]
	ds_write_b128 v211, v[198:201]
	ds_write_b128 v212, v[202:205]
	ds_write_b128 v213, v[206:209]
	ds_read_b128 v[218:221], v241 offset:16384
	ds_read_b128 v[222:225], v241 offset:17408
	ds_read_b128 v[210:213], v241 offset:18432
	ds_read_b128 v[214:217], v241 offset:19456
	ds_read_b128 v[202:205], v241 offset:20480
	ds_read_b128 v[206:209], v241 offset:21504
	ds_read_b128 v[194:197], v241 offset:22528
	ds_read_b128 v[198:201], v241 offset:23552
	v_readlane_b32 s2, v255, 13
	v_readlane_b32 s3, v255, 14
	s_add_u32 s26, s2, s8
	s_mov_b32 m0, s40
	v_cndmask_b32_e64 v226, v226, v242, s[4:5]
	s_addc_u32 s27, s3, 0
	v_cndmask_b32_e64 v228, v228, v243, s[4:5]
	global_load_lds_dwordx4 v226, s[26:27]
	s_mov_b32 m0, s41
	v_cndmask_b32_e64 v229, 0, 1, s[24:25]
	global_load_lds_dwordx4 v228, s[26:27]
	s_waitcnt vmcnt(12)
	s_waitcnt lgkmcnt(0)
	v_cmp_ne_u32_e64 s[2:3], 1, v229
	s_andn2_b64 vcc, exec, s[24:25]
	s_barrier
	s_cbranch_vccnz .LBB0_4717
	s_setprio 1
	s_waitcnt lgkmcnt(0)
	v_mfma_f32_16x16x32_bf16 v[94:97], v[178:181], v[218:221], v[94:97]
	v_mfma_f32_16x16x32_bf16 v[90:93], v[186:189], v[218:221], v[90:93]
	v_mfma_f32_16x16x32_bf16 v[78:81], v[178:181], v[210:213], v[78:81]
	v_mfma_f32_16x16x32_bf16 v[74:77], v[186:189], v[210:213], v[74:77]
	v_mfma_f32_16x16x32_bf16 v[62:65], v[178:181], v[202:205], v[62:65]
	v_mfma_f32_16x16x32_bf16 v[58:61], v[186:189], v[202:205], v[58:61]
	v_mfma_f32_16x16x32_bf16 v[46:49], v[178:181], v[194:197], v[46:49]
	v_mfma_f32_16x16x32_bf16 v[42:45], v[186:189], v[194:197], v[42:45]
	v_mfma_f32_16x16x32_bf16 v[94:97], v[182:185], v[222:225], v[94:97]
	v_mfma_f32_16x16x32_bf16 v[90:93], v[190:193], v[222:225], v[90:93]
	v_mfma_f32_16x16x32_bf16 v[78:81], v[182:185], v[214:217], v[78:81]
	v_mfma_f32_16x16x32_bf16 v[74:77], v[190:193], v[214:217], v[74:77]
	v_mfma_f32_16x16x32_bf16 v[62:65], v[182:185], v[206:209], v[62:65]
	v_mfma_f32_16x16x32_bf16 v[58:61], v[190:193], v[206:209], v[58:61]
	v_mfma_f32_16x16x32_bf16 v[46:49], v[182:185], v[198:201], v[46:49]
	v_mfma_f32_16x16x32_bf16 v[42:45], v[190:193], v[198:201], v[42:45]
	s_setprio 0
	s_setprio 1
	v_mfma_f32_16x16x32_bf16 v[86:89], v[162:165], v[218:221], v[86:89]
	v_mfma_f32_16x16x32_bf16 v[82:85], v[170:173], v[218:221], v[82:85]
	v_mfma_f32_16x16x32_bf16 v[70:73], v[162:165], v[210:213], v[70:73]
	v_mfma_f32_16x16x32_bf16 v[66:69], v[170:173], v[210:213], v[66:69]
	v_mfma_f32_16x16x32_bf16 v[54:57], v[162:165], v[202:205], v[54:57]
	v_mfma_f32_16x16x32_bf16 v[50:53], v[170:173], v[202:205], v[50:53]
	v_mfma_f32_16x16x32_bf16 v[38:41], v[162:165], v[194:197], v[38:41]
	v_mfma_f32_16x16x32_bf16 v[34:37], v[170:173], v[194:197], v[34:37]
	v_mfma_f32_16x16x32_bf16 v[86:89], v[166:169], v[222:225], v[86:89]
	v_mfma_f32_16x16x32_bf16 v[82:85], v[174:177], v[222:225], v[82:85]
	v_mfma_f32_16x16x32_bf16 v[70:73], v[166:169], v[214:217], v[70:73]
	v_mfma_f32_16x16x32_bf16 v[66:69], v[174:177], v[214:217], v[66:69]
	v_mfma_f32_16x16x32_bf16 v[54:57], v[166:169], v[206:209], v[54:57]
	v_mfma_f32_16x16x32_bf16 v[50:53], v[174:177], v[206:209], v[50:53]
	v_mfma_f32_16x16x32_bf16 v[38:41], v[166:169], v[198:201], v[38:41]
	v_mfma_f32_16x16x32_bf16 v[34:37], v[174:177], v[198:201], v[34:37]
	s_setprio 0
; #define PG8_BWAIT(n) asm volatile("s_waitcnt vmcnt(" #n ")" : "+v"(bv[0]), "+v"(bv[1]), "+v"(bv[2]), "+v"(bv[3]), "+v"(bv[4]), "+v"(bv[5]), "+v"(bv[6]), "+v"(bv[7]) :: "memory")
; #define PG8_STAGE_A(bufoff, V0, V1, kb) do { \
;         __builtin_amdgcn_global_load_lds((const unsigned*)((Abase + (kb)) + (V0)), (LAS unsigned*)(lds + (bufoff) + ldsw), 16, 0, 0); \
;         __builtin_amdgcn_global_load_lds((const unsigned*)((Abase + (kb)) + (V1)), (LAS unsigned*)(lds + (bufoff) + ldsw + 8192), 16, 0, 0); } while (0)
; #define PG8_LDA(dst, b, h) do { _Pragma("unroll") for (int m = 0; m < 4; ++m) _Pragma("unroll") for (int k = 0; k < 2; ++k) dst[m][k] = *(const LAS bf16x8*)(lds + PG8_SA(b, h) + aoff + m * 2048 + k * 1024); } while (0)
; #define PG8_LDB(dst, b, h) do { _Pragma("unroll") for (int n = 0; n < 2; ++n) _Pragma("unroll") for (int k = 0; k < 2; ++k) dst[n][k] = *(const LAS bf16x8*)(lds + PG8_SB(b, h) + boff + n * 2048 + k * 1024); } while (0)
; #define PG8_MMA(ai, bj, At, Bt) do { __builtin_amdgcn_s_setprio(1); _Pragma("unroll") for (int m = 0; m < 4; ++m) _Pragma("unroll") for (int n = 0; n < 2; ++n) _Pragma("unroll") for (int k = 0; k < 2; ++k) \
;         acc[ai][bj][m][n] = __builtin_amdgcn_mfma_f32_16x16x32_bf16(Bt[n][k], At[m][k], acc[ai][bj][m][n], 0, 0, 0); __builtin_amdgcn_s_setprio(0); } while (0)
; #define PG8_WAIT_V(n) asm volatile("s_waitcnt vmcnt(" #n ")" ::: "memory")
; #define PG8_WAIT_L(n) asm volatile("s_waitcnt lgkmcnt(" #n ")" ::: "memory")
; #define PG8_BAR __builtin_amdgcn_s_barrier()
; #define PG8_SCHED __builtin_amdgcn_sched_barrier(0)
; template <class Epi, class Sched, bool ALIGN_EPI>
; __device__ __forceinline__ void gemm_phase(LAS unsigned char* lds, const Gemm g, const Sched& S, const Epi& E) {
;     ...
;             PG8_LDB(B0, 1, 0); PG8_LDB(B1, 1, 1); PG8_SCHED; PG8_LDA(At, 1, 0); PG8_STAGE_A(PG8_SA(0, 1), vc10, vc11, kb2);
;             PG8_WAIT_V(12); PG8_WAIT_L(0); PG8_BAR; PG8_MMA(0, 0, At, B0); PG8_MMA(0, 1, At, B1); PG8_BAR; PG8_SCHED;
;             PG8_BWAIT(2); PG8_BCOMMIT(1); PG8_SCHED; PG8_LDA(At, 1, 1); PG8_BISSUE(t + 4 >= nt ? pbn + (size_t)(t + 4 - nt) * 64 * Sched::LDN : pbc + (size_t)(t + 4) * 64 * Sched::LDN); PG8_STAGE_A(PG8_SA(1, 0), vc00, vc01, kb2 + 128u);
.LBB0_4717:
	v_cndmask_b32_e64 v234, v234, v245, s[4:5]
	v_cndmask_b32_e64 v233, v233, v244, s[4:5]
	s_barrier
	v_add_u32_e32 v162, 0x18000, v240
	v_add_u32_e32 v174, 0x1c000, v240
	ds_read_b128 v[178:181], v162
	ds_read_b128 v[182:185], v162 offset:1024
	ds_read_b128 v[186:189], v162 offset:2048
	ds_read_b128 v[190:193], v162 offset:3072
	ds_read_b128 v[162:165], v174
	ds_read_b128 v[166:169], v174 offset:1024
	ds_read_b128 v[170:173], v174 offset:2048
	ds_read_b128 v[174:177], v174 offset:3072
	s_mov_b32 m0, s42
	s_waitcnt lgkmcnt(0)
	ds_read_b128 v[194:197], v241 offset:32768
	ds_read_b128 v[198:201], v241 offset:33792
	ds_read_b128 v[202:205], v241 offset:34816
	ds_read_b128 v[206:209], v241 offset:35840
	ds_read_b128 v[210:213], v241 offset:36864
	ds_read_b128 v[214:217], v241 offset:37888
	ds_read_b128 v[218:221], v241 offset:38912
	ds_read_b128 v[222:225], v241 offset:39936
	global_load_lds_dwordx4 v233, s[26:27]
	s_mov_b32 m0, s43
	s_nop 0
	global_load_lds_dwordx4 v234, s[26:27]
	s_waitcnt vmcnt(12)
	s_waitcnt lgkmcnt(0)
	s_barrier
	s_setprio 1
	s_waitcnt lgkmcnt(0)
	v_mfma_f32_16x16x32_bf16 v[158:161], v[178:181], v[194:197], v[158:161]
	v_mfma_f32_16x16x32_bf16 v[154:157], v[186:189], v[194:197], v[154:157]
	v_mfma_f32_16x16x32_bf16 v[142:145], v[178:181], v[202:205], v[142:145]
	v_mfma_f32_16x16x32_bf16 v[138:141], v[186:189], v[202:205], v[138:141]
	v_mfma_f32_16x16x32_bf16 v[126:129], v[178:181], v[210:213], v[126:129]
	v_mfma_f32_16x16x32_bf16 v[122:125], v[186:189], v[210:213], v[122:125]
	v_mfma_f32_16x16x32_bf16 v[110:113], v[178:181], v[218:221], v[110:113]
	v_mfma_f32_16x16x32_bf16 v[106:109], v[186:189], v[218:221], v[106:109]
	v_mfma_f32_16x16x32_bf16 v[158:161], v[182:185], v[198:201], v[158:161]
	v_mfma_f32_16x16x32_bf16 v[154:157], v[190:193], v[198:201], v[154:157]
	v_mfma_f32_16x16x32_bf16 v[142:145], v[182:185], v[206:209], v[142:145]
	v_mfma_f32_16x16x32_bf16 v[138:141], v[190:193], v[206:209], v[138:141]
	v_mfma_f32_16x16x32_bf16 v[126:129], v[182:185], v[214:217], v[126:129]
	v_mfma_f32_16x16x32_bf16 v[122:125], v[190:193], v[214:217], v[122:125]
	v_mfma_f32_16x16x32_bf16 v[110:113], v[182:185], v[222:225], v[110:113]
	v_mfma_f32_16x16x32_bf16 v[106:109], v[190:193], v[222:225], v[106:109]
	s_setprio 0
	s_setprio 1
	v_mfma_f32_16x16x32_bf16 v[150:153], v[162:165], v[194:197], v[150:153]
	v_mfma_f32_16x16x32_bf16 v[146:149], v[170:173], v[194:197], v[146:149]
	v_mfma_f32_16x16x32_bf16 v[134:137], v[162:165], v[202:205], v[134:137]
	v_mfma_f32_16x16x32_bf16 v[130:133], v[170:173], v[202:205], v[130:133]
	v_mfma_f32_16x16x32_bf16 v[118:121], v[162:165], v[210:213], v[118:121]
	v_mfma_f32_16x16x32_bf16 v[114:117], v[170:173], v[210:213], v[114:117]
	v_mfma_f32_16x16x32_bf16 v[102:105], v[162:165], v[218:221], v[102:105]
	v_mfma_f32_16x16x32_bf16 v[98:101], v[170:173], v[218:221], v[98:101]
	v_mfma_f32_16x16x32_bf16 v[150:153], v[166:169], v[198:201], v[150:153]
	v_mfma_f32_16x16x32_bf16 v[146:149], v[174:177], v[198:201], v[146:149]
	v_mfma_f32_16x16x32_bf16 v[134:137], v[166:169], v[206:209], v[134:137]
	v_mfma_f32_16x16x32_bf16 v[130:133], v[174:177], v[206:209], v[130:133]
	v_mfma_f32_16x16x32_bf16 v[118:121], v[166:169], v[214:217], v[118:121]
	v_mfma_f32_16x16x32_bf16 v[114:117], v[174:177], v[214:217], v[114:117]
	v_mfma_f32_16x16x32_bf16 v[102:105], v[166:169], v[222:225], v[102:105]
	v_mfma_f32_16x16x32_bf16 v[98:101], v[174:177], v[222:225], v[98:101]
	s_setprio 0
	s_barrier
	s_waitcnt vmcnt(2)
	s_nop 0
	v_add_u32_e32 v210, 0x18000, v235
	v_cvt_pk_bf16_f32 v194, v2, v6
	v_cvt_pk_bf16_f32 v195, v10, v14
	v_cvt_pk_bf16_f32 v196, v18, v22
	v_cvt_pk_bf16_f32 v197, v26, v30
	v_cvt_pk_bf16_f32 v198, v3, v7
	v_cvt_pk_bf16_f32 v199, v11, v15
	v_cvt_pk_bf16_f32 v200, v19, v23
	v_cvt_pk_bf16_f32 v201, v27, v31
	v_cvt_pk_bf16_f32 v202, v4, v8
	v_cvt_pk_bf16_f32 v203, v12, v16
	v_cvt_pk_bf16_f32 v204, v20, v24
	v_cvt_pk_bf16_f32 v205, v28, v32
	v_cvt_pk_bf16_f32 v206, v5, v9
	v_cvt_pk_bf16_f32 v207, v13, v17
	v_cvt_pk_bf16_f32 v208, v21, v25
	v_cvt_pk_bf16_f32 v209, v29, v33
	v_xor_b32_e32 v211, 64, v210
	v_xor_b32_e32 v212, 0x80, v210
	v_xor_b32_e32 v213, 0xc0, v210
	s_cmp_lt_u32 s54, 12
	s_mov_b64 s[28:29], -1
	s_cbranch_scc0 .LBB0_4719
	s_add_u32 s4, s20, 0x40000
	s_addc_u32 s5, s21, 0
	s_mov_b64 s[28:29], 0

; #define PG8_BWAIT(n) asm volatile("s_waitcnt vmcnt(" #n ")" : "+v"(bv[0]), "+v"(bv[1]), "+v"(bv[2]), "+v"(bv[3]), "+v"(bv[4]), "+v"(bv[5]), "+v"(bv[6]), "+v"(bv[7]) :: "memory")
; #define PG8_STAGE_A(bufoff, V0, V1, kb) do { \
;         __builtin_amdgcn_global_load_lds((const unsigned*)((Abase + (kb)) + (V0)), (LAS unsigned*)(lds + (bufoff) + ldsw), 16, 0, 0); \
;         __builtin_amdgcn_global_load_lds((const unsigned*)((Abase + (kb)) + (V1)), (LAS unsigned*)(lds + (bufoff) + ldsw + 8192), 16, 0, 0); } while (0)
; #define PG8_LDA(dst, b, h) do { _Pragma("unroll") for (int m = 0; m < 4; ++m) _Pragma("unroll") for (int k = 0; k < 2; ++k) dst[m][k] = *(const LAS bf16x8*)(lds + PG8_SA(b, h) + aoff + m * 2048 + k * 1024); } while (0)
; #define PG8_MMA(ai, bj, At, Bt) do { __builtin_amdgcn_s_setprio(1); _Pragma("unroll") for (int m = 0; m < 4; ++m) _Pragma("unroll") for (int n = 0; n < 2; ++n) _Pragma("unroll") for (int k = 0; k < 2; ++k) \
;         acc[ai][bj][m][n] = __builtin_amdgcn_mfma_f32_16x16x32_bf16(Bt[n][k], At[m][k], acc[ai][bj][m][n], 0, 0, 0); __builtin_amdgcn_s_setprio(0); } while (0)
; #define PG8_WAIT_V(n) asm volatile("s_waitcnt vmcnt(" #n ")" ::: "memory")
; #define PG8_WAIT_L(n) asm volatile("s_waitcnt lgkmcnt(" #n ")" ::: "memory")
; #define PG8_BAR __builtin_amdgcn_s_barrier()
; #define PG8_SCHED __builtin_amdgcn_sched_barrier(0)
; template <class Epi, class Sched, bool ALIGN_EPI>
; __device__ __forceinline__ void gemm_phase(LAS unsigned char* lds, const Gemm g, const Sched& S, const Epi& E) {
;     ...
;             PG8_BWAIT(2); PG8_BCOMMIT(1); PG8_SCHED; PG8_LDA(At, 1, 1); PG8_BISSUE(t + 4 >= nt ? pbn + (size_t)(t + 4 - nt) * 64 * Sched::LDN : pbc + (size_t)(t + 4) * 64 * Sched::LDN); PG8_STAGE_A(PG8_SA(1, 0), vc00, vc01, kb2 + 128u);
;             PG8_WAIT_V(12); PG8_WAIT_L(0); PG8_BAR; if (half1) { PG8_MMA(1, 0, At, B0); PG8_MMA(1, 1, At, B1); } PG8_BAR; PG8_SCHED;
.LBB0_4721:
	global_load_dwordx4 v[2:5], v232, s[4:5] offset:0
	global_load_dwordx4 v[6:9], v232, s[4:5] offset:0x400
	global_load_dwordx4 v[10:13], v232, s[4:5] offset:0x800
	global_load_dwordx4 v[14:17], v232, s[4:5] offset:0xc00
	s_add_u32 s4, s4, 0x1000
	s_addc_u32 s5, s5, 0
	global_load_dwordx4 v[18:21], v232, s[4:5] offset:0
	global_load_dwordx4 v[22:25], v232, s[4:5] offset:0x400
	v_lshl_add_u64 v[246:247], s[26:27], 0, v[226:227]
	v_mov_b32_e32 v229, v227
	global_load_dwordx4 v[26:29], v232, s[4:5] offset:0x800
	s_mov_b32 m0, s44
	v_lshl_add_u64 v[248:249], s[26:27], 0, v[228:229]
	global_load_dwordx4 v[30:33], v232, s[4:5] offset:0xc00
	ds_write_b128 v210, v[194:197]
	ds_write_b128 v211, v[198:201]
	ds_write_b128 v212, v[202:205]
	ds_write_b128 v213, v[206:209]
	ds_read_b128 v[218:221], v241 offset:49152
	ds_read_b128 v[222:225], v241 offset:50176
	ds_read_b128 v[210:213], v241 offset:51200
	ds_read_b128 v[214:217], v241 offset:52224
	ds_read_b128 v[202:205], v241 offset:53248
	ds_read_b128 v[206:209], v241 offset:54272
	ds_read_b128 v[194:197], v241 offset:55296
	ds_read_b128 v[198:201], v241 offset:56320
	v_lshl_add_u64 v[246:247], v[246:247], 0, s[12:13]
	global_load_lds_dwordx4 v[246:247], off
	v_lshl_add_u64 v[246:247], v[248:249], 0, s[12:13]
	s_mov_b32 m0, s45
	s_and_b64 vcc, exec, s[2:3]
	global_load_lds_dwordx4 v[246:247], off
	s_waitcnt vmcnt(12)
	s_waitcnt lgkmcnt(0)
	s_barrier
	s_cbranch_vccnz .LBB0_4723
	s_setprio 1
	s_waitcnt lgkmcnt(0)
	v_mfma_f32_16x16x32_bf16 v[94:97], v[178:181], v[218:221], v[94:97]
	v_mfma_f32_16x16x32_bf16 v[90:93], v[186:189], v[218:221], v[90:93]
	v_mfma_f32_16x16x32_bf16 v[78:81], v[178:181], v[210:213], v[78:81]
	v_mfma_f32_16x16x32_bf16 v[74:77], v[186:189], v[210:213], v[74:77]
	v_mfma_f32_16x16x32_bf16 v[62:65], v[178:181], v[202:205], v[62:65]
	v_mfma_f32_16x16x32_bf16 v[58:61], v[186:189], v[202:205], v[58:61]
	v_mfma_f32_16x16x32_bf16 v[46:49], v[178:181], v[194:197], v[46:49]
	v_mfma_f32_16x16x32_bf16 v[42:45], v[186:189], v[194:197], v[42:45]
	v_mfma_f32_16x16x32_bf16 v[94:97], v[182:185], v[222:225], v[94:97]
	v_mfma_f32_16x16x32_bf16 v[90:93], v[190:193], v[222:225], v[90:93]
	v_mfma_f32_16x16x32_bf16 v[78:81], v[182:185], v[214:217], v[78:81]
	v_mfma_f32_16x16x32_bf16 v[74:77], v[190:193], v[214:217], v[74:77]
	v_mfma_f32_16x16x32_bf16 v[62:65], v[182:185], v[206:209], v[62:65]
	v_mfma_f32_16x16x32_bf16 v[58:61], v[190:193], v[206:209], v[58:61]
	v_mfma_f32_16x16x32_bf16 v[46:49], v[182:185], v[198:201], v[46:49]
	v_mfma_f32_16x16x32_bf16 v[42:45], v[190:193], v[198:201], v[42:45]
	s_setprio 0
	s_setprio 1
	v_mfma_f32_16x16x32_bf16 v[86:89], v[162:165], v[218:221], v[86:89]
	v_mfma_f32_16x16x32_bf16 v[82:85], v[170:173], v[218:221], v[82:85]
	v_mfma_f32_16x16x32_bf16 v[70:73], v[162:165], v[210:213], v[70:73]
	v_mfma_f32_16x16x32_bf16 v[66:69], v[170:173], v[210:213], v[66:69]
	v_mfma_f32_16x16x32_bf16 v[54:57], v[162:165], v[202:205], v[54:57]
	v_mfma_f32_16x16x32_bf16 v[50:53], v[170:173], v[202:205], v[50:53]
	v_mfma_f32_16x16x32_bf16 v[38:41], v[162:165], v[194:197], v[38:41]
	v_mfma_f32_16x16x32_bf16 v[34:37], v[170:173], v[194:197], v[34:37]
	v_mfma_f32_16x16x32_bf16 v[86:89], v[166:169], v[222:225], v[86:89]
	v_mfma_f32_16x16x32_bf16 v[82:85], v[174:177], v[222:225], v[82:85]
	v_mfma_f32_16x16x32_bf16 v[70:73], v[166:169], v[214:217], v[70:73]
	v_mfma_f32_16x16x32_bf16 v[66:69], v[174:177], v[214:217], v[66:69]
	v_mfma_f32_16x16x32_bf16 v[54:57], v[166:169], v[206:209], v[54:57]
	v_mfma_f32_16x16x32_bf16 v[50:53], v[174:177], v[206:209], v[50:53]
	v_mfma_f32_16x16x32_bf16 v[38:41], v[166:169], v[198:201], v[38:41]
	v_mfma_f32_16x16x32_bf16 v[34:37], v[174:177], v[198:201], v[34:37]
	s_setprio 0

; #define PG8_BWAIT(n) asm volatile("s_waitcnt vmcnt(" #n ")" : "+v"(bv[0]), "+v"(bv[1]), "+v"(bv[2]), "+v"(bv[3]), "+v"(bv[4]), "+v"(bv[5]), "+v"(bv[6]), "+v"(bv[7]) :: "memory")
; #define PG8_STAGE_A(bufoff, V0, V1, kb) do { \
;         __builtin_amdgcn_global_load_lds((const unsigned*)((Abase + (kb)) + (V0)), (LAS unsigned*)(lds + (bufoff) + ldsw), 16, 0, 0); \
;         __builtin_amdgcn_global_load_lds((const unsigned*)((Abase + (kb)) + (V1)), (LAS unsigned*)(lds + (bufoff) + ldsw + 8192), 16, 0, 0); } while (0)
; #define PG8_LDA(dst, b, h) do { _Pragma("unroll") for (int m = 0; m < 4; ++m) _Pragma("unroll") for (int k = 0; k < 2; ++k) dst[m][k] = *(const LAS bf16x8*)(lds + PG8_SA(b, h) + aoff + m * 2048 + k * 1024); } while (0)
; #define PG8_LDB(dst, b, h) do { _Pragma("unroll") for (int n = 0; n < 2; ++n) _Pragma("unroll") for (int k = 0; k < 2; ++k) dst[n][k] = *(const LAS bf16x8*)(lds + PG8_SB(b, h) + boff + n * 2048 + k * 1024); } while (0)
; #define PG8_MMA(ai, bj, At, Bt) do { __builtin_amdgcn_s_setprio(1); _Pragma("unroll") for (int m = 0; m < 4; ++m) _Pragma("unroll") for (int n = 0; n < 2; ++n) _Pragma("unroll") for (int k = 0; k < 2; ++k) \
;         acc[ai][bj][m][n] = __builtin_amdgcn_mfma_f32_16x16x32_bf16(Bt[n][k], At[m][k], acc[ai][bj][m][n], 0, 0, 0); __builtin_amdgcn_s_setprio(0); } while (0)
; #define PG8_WAIT_V(n) asm volatile("s_waitcnt vmcnt(" #n ")" ::: "memory")
; #define PG8_WAIT_L(n) asm volatile("s_waitcnt lgkmcnt(" #n ")" ::: "memory")
; #define PG8_BAR __builtin_amdgcn_s_barrier()
; template <class Epi, class Sched, bool ALIGN_EPI>
; __device__ __forceinline__ void gemm_phase(LAS unsigned char* lds, const Gemm g, const Sched& S, const Epi& E) {
;     ...
;             PG8_LDB(B0, 0, 0); PG8_LDB(B1, 0, 1); PG8_SCHED; PG8_LDA(At, 0, 0); PG8_STAGE_A(PG8_SA(1, 1), vc10, vc11, kb1);
;             PG8_WAIT_V(12); PG8_WAIT_L(0); PG8_BAR; PG8_MMA(0, 0, At, B0); PG8_MMA(0, 1, At, B1); PG8_BAR; PG8_SCHED;
;             if (last) { vc10 = vn10; vc11 = vn11; }
;             PG8_BWAIT(2); PG8_BCOMMIT(0); PG8_SCHED; PG8_LDA(At, 0, 1); PG8_BISSUE(t + 3 >= nt ? pbn + (size_t)(t + 3 - nt) * 64 * Sched::LDN : pbc + (size_t)(t + 3) * 64 * Sched::LDN); PG8_STAGE_A(PG8_SA(0, 0), vc00, vc01, kb2);
;             PG8_WAIT_V(12); PG8_WAIT_L(0); PG8_BAR; if (half1) { PG8_MMA(1, 0, At, B0); PG8_MMA(1, 1, At, B1); } PG8_BAR; PG8_SCHED;
.LBB0_4908:
	v_add_u32_e32 v162, 0x10000, v247
	v_add_u32_e32 v174, 0x14000, v247
	ds_read_b128 v[178:181], v162
	ds_read_b128 v[182:185], v162 offset:1024
	ds_read_b128 v[186:189], v162 offset:2048
	ds_read_b128 v[190:193], v162 offset:3072
	ds_read_b128 v[162:165], v174
	ds_read_b128 v[166:169], v174 offset:1024
	ds_read_b128 v[170:173], v174 offset:2048
	ds_read_b128 v[174:177], v174 offset:3072
	s_lshl_b32 s3, s52, 7
	s_add_i32 s2, s3, 0x100
	v_cndmask_b32_e64 v228, v228, v250, s[28:29]
	v_readlane_b32 s56, v254, 53
	v_readlane_b32 s57, v254, 54
	s_add_u32 s30, s56, s3
	s_addc_u32 s31, s57, 0
	v_lshl_add_u64 v[236:237], s[30:31], 0, v[230:231]
	v_lshl_add_u64 v[236:237], v[236:237], 0, s[14:15]
	s_add_i32 m0, s37, 0xc000
	v_mov_b32_e32 v233, v231
	s_waitcnt lgkmcnt(0)
	ds_read_b128 v[194:197], v248
	ds_read_b128 v[198:201], v248 offset:1024
	ds_read_b128 v[202:205], v248 offset:2048
	ds_read_b128 v[206:209], v248 offset:3072
	ds_read_b128 v[210:213], v248 offset:4096
	ds_read_b128 v[214:217], v248 offset:5120
	ds_read_b128 v[218:221], v248 offset:6144
	ds_read_b128 v[222:225], v248 offset:7168
	global_load_lds_dwordx4 v[236:237], off
	v_lshl_add_u64 v[236:237], s[30:31], 0, v[232:233]
	v_lshl_add_u64 v[236:237], v[236:237], 0, s[14:15]
	s_add_i32 m0, s37, 0xe000
	s_nop 0
	global_load_lds_dwordx4 v[236:237], off
	s_waitcnt vmcnt(12)
	s_waitcnt lgkmcnt(0)
	s_barrier
	s_setprio 1
	s_waitcnt lgkmcnt(0)
	v_mfma_f32_16x16x32_bf16 v[158:161], v[178:181], v[194:197], v[158:161]
	v_mfma_f32_16x16x32_bf16 v[154:157], v[186:189], v[194:197], v[154:157]
	v_mfma_f32_16x16x32_bf16 v[142:145], v[178:181], v[202:205], v[142:145]
	v_mfma_f32_16x16x32_bf16 v[138:141], v[186:189], v[202:205], v[138:141]
	v_mfma_f32_16x16x32_bf16 v[126:129], v[178:181], v[210:213], v[126:129]
	v_mfma_f32_16x16x32_bf16 v[122:125], v[186:189], v[210:213], v[122:125]
	v_mfma_f32_16x16x32_bf16 v[110:113], v[178:181], v[218:221], v[110:113]
	v_mfma_f32_16x16x32_bf16 v[106:109], v[186:189], v[218:221], v[106:109]
	v_mfma_f32_16x16x32_bf16 v[158:161], v[182:185], v[198:201], v[158:161]
	v_mfma_f32_16x16x32_bf16 v[154:157], v[190:193], v[198:201], v[154:157]
	v_mfma_f32_16x16x32_bf16 v[142:145], v[182:185], v[206:209], v[142:145]
	v_mfma_f32_16x16x32_bf16 v[138:141], v[190:193], v[206:209], v[138:141]
	v_mfma_f32_16x16x32_bf16 v[126:129], v[182:185], v[214:217], v[126:129]
	v_mfma_f32_16x16x32_bf16 v[122:125], v[190:193], v[214:217], v[122:125]
	v_mfma_f32_16x16x32_bf16 v[110:113], v[182:185], v[222:225], v[110:113]
	v_mfma_f32_16x16x32_bf16 v[106:109], v[190:193], v[222:225], v[106:109]
	s_setprio 0
	s_setprio 1
	v_mfma_f32_16x16x32_bf16 v[150:153], v[162:165], v[194:197], v[150:153]
	v_mfma_f32_16x16x32_bf16 v[146:149], v[170:173], v[194:197], v[146:149]
	v_mfma_f32_16x16x32_bf16 v[134:137], v[162:165], v[202:205], v[134:137]
	v_mfma_f32_16x16x32_bf16 v[130:133], v[170:173], v[202:205], v[130:133]
	v_mfma_f32_16x16x32_bf16 v[118:121], v[162:165], v[210:213], v[118:121]
	v_mfma_f32_16x16x32_bf16 v[114:117], v[170:173], v[210:213], v[114:117]
	v_mfma_f32_16x16x32_bf16 v[102:105], v[162:165], v[218:221], v[102:105]
	v_mfma_f32_16x16x32_bf16 v[98:101], v[170:173], v[218:221], v[98:101]
	v_mfma_f32_16x16x32_bf16 v[150:153], v[166:169], v[198:201], v[150:153]
	v_mfma_f32_16x16x32_bf16 v[146:149], v[174:177], v[198:201], v[146:149]
	v_mfma_f32_16x16x32_bf16 v[134:137], v[166:169], v[206:209], v[134:137]
	v_mfma_f32_16x16x32_bf16 v[130:133], v[174:177], v[206:209], v[130:133]
	v_mfma_f32_16x16x32_bf16 v[118:121], v[166:169], v[214:217], v[118:121]
	v_mfma_f32_16x16x32_bf16 v[114:117], v[174:177], v[214:217], v[114:117]
	v_mfma_f32_16x16x32_bf16 v[102:105], v[166:169], v[222:225], v[102:105]
	v_mfma_f32_16x16x32_bf16 v[98:101], v[174:177], v[222:225], v[98:101]
	s_setprio 0
	s_barrier
	s_waitcnt vmcnt(2)
	v_cndmask_b32_e64 v226, v226, v249, s[28:29]
	v_add_u32_e32 v210, 0x10000, v242
	v_cvt_pk_bf16_f32 v194, v2, v6
	v_cvt_pk_bf16_f32 v195, v10, v14
	v_cvt_pk_bf16_f32 v196, v18, v22
	v_cvt_pk_bf16_f32 v197, v26, v30
	v_cvt_pk_bf16_f32 v198, v3, v7
	v_cvt_pk_bf16_f32 v199, v11, v15
	v_cvt_pk_bf16_f32 v200, v19, v23
	v_cvt_pk_bf16_f32 v201, v27, v31
	v_cvt_pk_bf16_f32 v202, v4, v8
	v_cvt_pk_bf16_f32 v203, v12, v16
	v_cvt_pk_bf16_f32 v204, v20, v24
	v_cvt_pk_bf16_f32 v205, v28, v32
	v_cvt_pk_bf16_f32 v206, v5, v9
	v_cvt_pk_bf16_f32 v207, v13, v17
	v_cvt_pk_bf16_f32 v208, v21, v25
	v_cvt_pk_bf16_f32 v209, v29, v33
	v_xor_b32_e32 v211, 64, v210
	v_xor_b32_e32 v212, 0x80, v210
	v_xor_b32_e32 v213, 0xc0, v210
	s_add_i32 s8, s52, -1
	s_lshl_b64 s[30:31], s[8:9], 18
	s_add_u32 s3, s49, s30
	s_addc_u32 s8, s21, s31
	s_and_b64 s[30:31], s[26:27], exec
	s_cselect_b32 s30, s50, s3
	s_cselect_b32 s31, s51, s8
	s_add_u32 s54, s30, 0x1000
	global_load_dwordx4 v[2:5], v240, s[30:31] offset:0
	s_addc_u32 s55, s31, 0
	global_load_dwordx4 v[6:9], v240, s[54:55] offset:0
	s_add_u32 s54, s30, 0x2000
	s_addc_u32 s55, s31, 0
	global_load_dwordx4 v[10:13], v240, s[54:55] offset:0
	s_add_u32 s54, s30, 0x3000
	s_addc_u32 s55, s31, 0
	global_load_dwordx4 v[14:17], v240, s[54:55] offset:0
	s_add_u32 s54, s30, 0x4000
	s_addc_u32 s55, s31, 0
	global_load_dwordx4 v[18:21], v240, s[54:55] offset:0
	s_add_u32 s54, s30, 0x5000
	s_addc_u32 s55, s31, 0
	global_load_dwordx4 v[22:25], v240, s[54:55] offset:0
	s_add_u32 s54, s30, 0x6000
	s_addc_u32 s55, s31, 0
	s_add_u32 s30, s30, 0x7000
	global_load_dwordx4 v[26:29], v240, s[54:55] offset:0
	s_addc_u32 s31, s31, 0
	global_load_dwordx4 v[30:33], v240, s[30:31] offset:0
	ds_write_b128 v210, v[194:197]
	ds_write_b128 v211, v[198:201]
	ds_write_b128 v212, v[202:205]
	ds_write_b128 v213, v[206:209]
	ds_read_b128 v[218:221], v248 offset:16384
	ds_read_b128 v[222:225], v248 offset:17408
	ds_read_b128 v[210:213], v248 offset:18432
	ds_read_b128 v[214:217], v248 offset:19456
	ds_read_b128 v[202:205], v248 offset:20480
	ds_read_b128 v[206:209], v248 offset:21504
	ds_read_b128 v[194:197], v248 offset:22528
	ds_read_b128 v[198:201], v248 offset:23552
	s_and_b64 s[30:31], s[28:29], exec
	s_cselect_b32 s2, 0, s2
	s_cselect_b32 s3, 0, 0
	s_add_u32 s30, s56, s2
	s_mov_b32 m0, s37
	s_addc_u32 s31, s57, s3
	global_load_lds_dwordx4 v226, s[30:31]
	s_mov_b32 m0, s38
	v_mov_b32_e32 v227, v231
	global_load_lds_dwordx4 v228, s[30:31]
	s_waitcnt vmcnt(12)
	s_waitcnt lgkmcnt(0)
	v_lshl_add_u64 v[238:239], s[30:31], 0, v[226:227]
	v_mov_b32_e32 v229, v231
	v_cndmask_b32_e64 v227, 0, 1, s[24:25]
	v_lshl_add_u64 v[236:237], s[30:31], 0, v[228:229]
	v_cmp_ne_u32_e64 s[2:3], 1, v227
	s_andn2_b64 vcc, exec, s[24:25]
	s_barrier
; #define PG8_STAGE_A(bufoff, V0, V1, kb) do { \
;         __builtin_amdgcn_global_load_lds((const unsigned*)((Abase + (kb)) + (V0)), (LAS unsigned*)(lds + (bufoff) + ldsw), 16, 0, 0); \
;         __builtin_amdgcn_global_load_lds((const unsigned*)((Abase + (kb)) + (V1)), (LAS unsigned*)(lds + (bufoff) + ldsw + 8192), 16, 0, 0); } while (0)
; #define PG8_LDA(dst, b, h) do { _Pragma("unroll") for (int m = 0; m < 4; ++m) _Pragma("unroll") for (int k = 0; k < 2; ++k) dst[m][k] = *(const LAS bf16x8*)(lds + PG8_SA(b, h) + aoff + m * 2048 + k * 1024); } while (0)
; #define PG8_LDB(dst, b, h) do { _Pragma("unroll") for (int n = 0; n < 2; ++n) _Pragma("unroll") for (int k = 0; k < 2; ++k) dst[n][k] = *(const LAS bf16x8*)(lds + PG8_SB(b, h) + boff + n * 2048 + k * 1024); } while (0)
; #define PG8_MMA(ai, bj, At, Bt) do { __builtin_amdgcn_s_setprio(1); _Pragma("unroll") for (int m = 0; m < 4; ++m) _Pragma("unroll") for (int n = 0; n < 2; ++n) _Pragma("unroll") for (int k = 0; k < 2; ++k) \
;         acc[ai][bj][m][n] = __builtin_amdgcn_mfma_f32_16x16x32_bf16(Bt[n][k], At[m][k], acc[ai][bj][m][n], 0, 0, 0); __builtin_amdgcn_s_setprio(0); } while (0)
; #define PG8_WAIT_V(n) asm volatile("s_waitcnt vmcnt(" #n ")" ::: "memory")
; #define PG8_WAIT_L(n) asm volatile("s_waitcnt lgkmcnt(" #n ")" ::: "memory")
; #define PG8_BAR __builtin_amdgcn_s_barrier()
; #define PG8_SCHED __builtin_amdgcn_sched_barrier(0)
; template <class Epi, class Sched, bool ALIGN_EPI>
; __device__ __forceinline__ void gemm_phase(LAS unsigned char* lds, const Gemm g, const Sched& S, const Epi& E) {
;     ...
;             PG8_WAIT_V(12); PG8_WAIT_L(0); PG8_BAR; if (half1) { PG8_MMA(1, 0, At, B0); PG8_MMA(1, 1, At, B1); } PG8_BAR; PG8_SCHED;
;             PG8_LDB(B0, 1, 0); PG8_LDB(B1, 1, 1); PG8_SCHED; PG8_LDA(At, 1, 0); PG8_STAGE_A(PG8_SA(0, 1), vc10, vc11, kb2);
;             PG8_WAIT_V(12); PG8_WAIT_L(0); PG8_BAR; PG8_MMA(0, 0, At, B0); PG8_MMA(0, 1, At, B1); PG8_BAR; PG8_SCHED;
	s_cbranch_vccnz .LBB0_4910
	s_setprio 1
	s_waitcnt lgkmcnt(0)
	v_mfma_f32_16x16x32_bf16 v[94:97], v[178:181], v[218:221], v[94:97]
	v_mfma_f32_16x16x32_bf16 v[90:93], v[186:189], v[218:221], v[90:93]
	v_mfma_f32_16x16x32_bf16 v[78:81], v[178:181], v[210:213], v[78:81]
	v_mfma_f32_16x16x32_bf16 v[74:77], v[186:189], v[210:213], v[74:77]
	v_mfma_f32_16x16x32_bf16 v[62:65], v[178:181], v[202:205], v[62:65]
	v_mfma_f32_16x16x32_bf16 v[58:61], v[186:189], v[202:205], v[58:61]
	v_mfma_f32_16x16x32_bf16 v[46:49], v[178:181], v[194:197], v[46:49]
	v_mfma_f32_16x16x32_bf16 v[42:45], v[186:189], v[194:197], v[42:45]
	v_mfma_f32_16x16x32_bf16 v[94:97], v[182:185], v[222:225], v[94:97]
	v_mfma_f32_16x16x32_bf16 v[90:93], v[190:193], v[222:225], v[90:93]
	v_mfma_f32_16x16x32_bf16 v[78:81], v[182:185], v[214:217], v[78:81]
	v_mfma_f32_16x16x32_bf16 v[74:77], v[190:193], v[214:217], v[74:77]
	v_mfma_f32_16x16x32_bf16 v[62:65], v[182:185], v[206:209], v[62:65]
	v_mfma_f32_16x16x32_bf16 v[58:61], v[190:193], v[206:209], v[58:61]
	v_mfma_f32_16x16x32_bf16 v[46:49], v[182:185], v[198:201], v[46:49]
	v_mfma_f32_16x16x32_bf16 v[42:45], v[190:193], v[198:201], v[42:45]
	s_setprio 0
	s_setprio 1
	v_mfma_f32_16x16x32_bf16 v[86:89], v[162:165], v[218:221], v[86:89]
	v_mfma_f32_16x16x32_bf16 v[82:85], v[170:173], v[218:221], v[82:85]
	v_mfma_f32_16x16x32_bf16 v[70:73], v[162:165], v[210:213], v[70:73]
	v_mfma_f32_16x16x32_bf16 v[66:69], v[170:173], v[210:213], v[66:69]
	v_mfma_f32_16x16x32_bf16 v[54:57], v[162:165], v[202:205], v[54:57]
	v_mfma_f32_16x16x32_bf16 v[50:53], v[170:173], v[202:205], v[50:53]
	v_mfma_f32_16x16x32_bf16 v[38:41], v[162:165], v[194:197], v[38:41]
	v_mfma_f32_16x16x32_bf16 v[34:37], v[170:173], v[194:197], v[34:37]
	v_mfma_f32_16x16x32_bf16 v[86:89], v[166:169], v[222:225], v[86:89]
	v_mfma_f32_16x16x32_bf16 v[82:85], v[174:177], v[222:225], v[82:85]
	v_mfma_f32_16x16x32_bf16 v[70:73], v[166:169], v[214:217], v[70:73]
	v_mfma_f32_16x16x32_bf16 v[66:69], v[174:177], v[214:217], v[66:69]
	v_mfma_f32_16x16x32_bf16 v[54:57], v[166:169], v[206:209], v[54:57]
	v_mfma_f32_16x16x32_bf16 v[50:53], v[174:177], v[206:209], v[50:53]
	v_mfma_f32_16x16x32_bf16 v[38:41], v[166:169], v[198:201], v[38:41]
	v_mfma_f32_16x16x32_bf16 v[34:37], v[174:177], v[198:201], v[34:37]
	s_setprio 0
.LBB0_4910:
	v_cndmask_b32_e64 v232, v232, v252, s[28:29]
	v_cndmask_b32_e64 v230, v230, v251, s[28:29]
	s_barrier
	v_add_u32_e32 v162, 0x18000, v247
	v_add_u32_e32 v174, 0x1c000, v247
	ds_read_b128 v[178:181], v162
	ds_read_b128 v[182:185], v162 offset:1024
	ds_read_b128 v[186:189], v162 offset:2048
	ds_read_b128 v[190:193], v162 offset:3072
	ds_read_b128 v[162:165], v174
	ds_read_b128 v[166:169], v174 offset:1024
	ds_read_b128 v[170:173], v174 offset:2048
	ds_read_b128 v[174:177], v174 offset:3072
	s_mov_b32 m0, s39
	s_waitcnt lgkmcnt(0)
	ds_read_b128 v[194:197], v248 offset:32768
	ds_read_b128 v[198:201], v248 offset:33792
	ds_read_b128 v[202:205], v248 offset:34816
	ds_read_b128 v[206:209], v248 offset:35840
	ds_read_b128 v[210:213], v248 offset:36864
	ds_read_b128 v[214:217], v248 offset:37888
	ds_read_b128 v[218:221], v248 offset:38912
	ds_read_b128 v[222:225], v248 offset:39936
	global_load_lds_dwordx4 v230, s[30:31]
	s_mov_b32 m0, s40
	s_nop 0
	global_load_lds_dwordx4 v232, s[30:31]
	s_waitcnt vmcnt(12)
	s_waitcnt lgkmcnt(0)
	s_barrier
	s_setprio 1
	s_waitcnt lgkmcnt(0)
	v_mfma_f32_16x16x32_bf16 v[158:161], v[178:181], v[194:197], v[158:161]
	v_mfma_f32_16x16x32_bf16 v[154:157], v[186:189], v[194:197], v[154:157]
	v_mfma_f32_16x16x32_bf16 v[142:145], v[178:181], v[202:205], v[142:145]
	v_mfma_f32_16x16x32_bf16 v[138:141], v[186:189], v[202:205], v[138:141]
	v_mfma_f32_16x16x32_bf16 v[126:129], v[178:181], v[210:213], v[126:129]
	v_mfma_f32_16x16x32_bf16 v[122:125], v[186:189], v[210:213], v[122:125]
	v_mfma_f32_16x16x32_bf16 v[110:113], v[178:181], v[218:221], v[110:113]
	v_mfma_f32_16x16x32_bf16 v[106:109], v[186:189], v[218:221], v[106:109]
	v_mfma_f32_16x16x32_bf16 v[158:161], v[182:185], v[198:201], v[158:161]
	v_mfma_f32_16x16x32_bf16 v[154:157], v[190:193], v[198:201], v[154:157]
	v_mfma_f32_16x16x32_bf16 v[142:145], v[182:185], v[206:209], v[142:145]
	v_mfma_f32_16x16x32_bf16 v[138:141], v[190:193], v[206:209], v[138:141]
	v_mfma_f32_16x16x32_bf16 v[126:129], v[182:185], v[214:217], v[126:129]
	v_mfma_f32_16x16x32_bf16 v[122:125], v[190:193], v[214:217], v[122:125]
	v_mfma_f32_16x16x32_bf16 v[110:113], v[182:185], v[222:225], v[110:113]
	v_mfma_f32_16x16x32_bf16 v[106:109], v[190:193], v[222:225], v[106:109]
	s_setprio 0
	s_setprio 1
	v_mfma_f32_16x16x32_bf16 v[150:153], v[162:165], v[194:197], v[150:153]
	v_mfma_f32_16x16x32_bf16 v[146:149], v[170:173], v[194:197], v[146:149]
	v_mfma_f32_16x16x32_bf16 v[134:137], v[162:165], v[202:205], v[134:137]
	v_mfma_f32_16x16x32_bf16 v[130:133], v[170:173], v[202:205], v[130:133]
	v_mfma_f32_16x16x32_bf16 v[118:121], v[162:165], v[210:213], v[118:121]
	v_mfma_f32_16x16x32_bf16 v[114:117], v[170:173], v[210:213], v[114:117]
	v_mfma_f32_16x16x32_bf16 v[102:105], v[162:165], v[218:221], v[102:105]
	v_mfma_f32_16x16x32_bf16 v[98:101], v[170:173], v[218:221], v[98:101]
	v_mfma_f32_16x16x32_bf16 v[150:153], v[166:169], v[198:201], v[150:153]
	v_mfma_f32_16x16x32_bf16 v[146:149], v[174:177], v[198:201], v[146:149]
	v_mfma_f32_16x16x32_bf16 v[134:137], v[166:169], v[206:209], v[134:137]
	v_mfma_f32_16x16x32_bf16 v[130:133], v[174:177], v[206:209], v[130:133]
	v_mfma_f32_16x16x32_bf16 v[118:121], v[166:169], v[214:217], v[118:121]
	v_mfma_f32_16x16x32_bf16 v[114:117], v[174:177], v[214:217], v[114:117]
	v_mfma_f32_16x16x32_bf16 v[102:105], v[166:169], v[222:225], v[102:105]
	v_mfma_f32_16x16x32_bf16 v[98:101], v[174:177], v[222:225], v[98:101]
	s_setprio 0
	s_barrier
; #define PG8_BWAIT(n) asm volatile("s_waitcnt vmcnt(" #n ")" : "+v"(bv[0]), "+v"(bv[1]), "+v"(bv[2]), "+v"(bv[3]), "+v"(bv[4]), "+v"(bv[5]), "+v"(bv[6]), "+v"(bv[7]) :: "memory")
; #define PG8_STAGE_A(bufoff, V0, V1, kb) do { \
;         __builtin_amdgcn_global_load_lds((const unsigned*)((Abase + (kb)) + (V0)), (LAS unsigned*)(lds + (bufoff) + ldsw), 16, 0, 0); \
;         __builtin_amdgcn_global_load_lds((const unsigned*)((Abase + (kb)) + (V1)), (LAS unsigned*)(lds + (bufoff) + ldsw + 8192), 16, 0, 0); } while (0)
; #define PG8_LDA(dst, b, h) do { _Pragma("unroll") for (int m = 0; m < 4; ++m) _Pragma("unroll") for (int k = 0; k < 2; ++k) dst[m][k] = *(const LAS bf16x8*)(lds + PG8_SA(b, h) + aoff + m * 2048 + k * 1024); } while (0)
; #define PG8_MMA(ai, bj, At, Bt) do { __builtin_amdgcn_s_setprio(1); _Pragma("unroll") for (int m = 0; m < 4; ++m) _Pragma("unroll") for (int n = 0; n < 2; ++n) _Pragma("unroll") for (int k = 0; k < 2; ++k) \
;         acc[ai][bj][m][n] = __builtin_amdgcn_mfma_f32_16x16x32_bf16(Bt[n][k], At[m][k], acc[ai][bj][m][n], 0, 0, 0); __builtin_amdgcn_s_setprio(0); } while (0)
; #define PG8_WAIT_V(n) asm volatile("s_waitcnt vmcnt(" #n ")" ::: "memory")
; #define PG8_WAIT_L(n) asm volatile("s_waitcnt lgkmcnt(" #n ")" ::: "memory")
; #define PG8_BAR __builtin_amdgcn_s_barrier()
; #define PG8_SCHED __builtin_amdgcn_sched_barrier(0)
; template <class Epi, class Sched, bool ALIGN_EPI>
; __device__ __forceinline__ void gemm_phase(LAS unsigned char* lds, const Gemm g, const Sched& S, const Epi& E) {
;     ...
;             PG8_BWAIT(2); PG8_BCOMMIT(1); PG8_SCHED; PG8_LDA(At, 1, 1); PG8_BISSUE(t + 4 >= nt ? pbn + (size_t)(t + 4 - nt) * 64 * Sched::LDN : pbc + (size_t)(t + 4) * 64 * Sched::LDN); PG8_STAGE_A(PG8_SA(1, 0), vc00, vc01, kb2 + 128u);
;             PG8_WAIT_V(12); PG8_WAIT_L(0); PG8_BAR; if (half1) { PG8_MMA(1, 0, At, B0); PG8_MMA(1, 1, At, B1); } PG8_BAR; PG8_SCHED;
	s_waitcnt vmcnt(2)
	s_nop 0
	v_add_u32_e32 v210, 0x18000, v242
	v_cvt_pk_bf16_f32 v194, v2, v6
	v_cvt_pk_bf16_f32 v195, v10, v14
	v_cvt_pk_bf16_f32 v196, v18, v22
	v_cvt_pk_bf16_f32 v197, v26, v30
	v_cvt_pk_bf16_f32 v198, v3, v7
	v_cvt_pk_bf16_f32 v199, v11, v15
	v_cvt_pk_bf16_f32 v200, v19, v23
	v_cvt_pk_bf16_f32 v201, v27, v31
	v_cvt_pk_bf16_f32 v202, v4, v8
	v_cvt_pk_bf16_f32 v203, v12, v16
	v_cvt_pk_bf16_f32 v204, v20, v24
	v_cvt_pk_bf16_f32 v205, v28, v32
	v_cvt_pk_bf16_f32 v206, v5, v9
	v_cvt_pk_bf16_f32 v207, v13, v17
	v_cvt_pk_bf16_f32 v208, v21, v25
	v_cvt_pk_bf16_f32 v209, v29, v33
	v_xor_b32_e32 v211, 64, v210
	v_xor_b32_e32 v212, 0x80, v210
	v_xor_b32_e32 v213, 0xc0, v210
	s_lshl_b32 s8, s52, 16
	s_lshl_b64 s[28:29], s[8:9], 2
	s_add_u32 s28, s49, s28
	s_addc_u32 s29, s21, s29
	s_add_u32 s30, s28, 0x1000
	global_load_dwordx4 v[2:5], v240, s[28:29] offset:0
	s_addc_u32 s31, s29, 0
	global_load_dwordx4 v[6:9], v240, s[30:31] offset:0
	s_add_u32 s30, s28, 0x2000
	s_addc_u32 s31, s29, 0
	global_load_dwordx4 v[10:13], v240, s[30:31] offset:0
	s_add_u32 s30, s28, 0x3000
	s_addc_u32 s31, s29, 0
	global_load_dwordx4 v[14:17], v240, s[30:31] offset:0
	s_add_u32 s30, s28, 0x4000
	s_addc_u32 s31, s29, 0
	global_load_dwordx4 v[18:21], v240, s[30:31] offset:0
	s_add_u32 s30, s28, 0x5000
	s_addc_u32 s31, s29, 0
	global_load_dwordx4 v[22:25], v240, s[30:31] offset:0
	s_add_u32 s30, s28, 0x6000
	s_addc_u32 s31, s29, 0
	global_load_dwordx4 v[26:29], v240, s[30:31] offset:0
	s_add_u32 s28, s28, 0x7000
	s_mov_b32 m0, s41
	s_addc_u32 s29, s29, 0
	global_load_dwordx4 v[30:33], v240, s[28:29] offset:0
	ds_write_b128 v210, v[194:197]
	ds_write_b128 v211, v[198:201]
	ds_write_b128 v212, v[202:205]
	ds_write_b128 v213, v[206:209]
	ds_read_b128 v[218:221], v248 offset:49152
	ds_read_b128 v[222:225], v248 offset:50176
	ds_read_b128 v[210:213], v248 offset:51200
	ds_read_b128 v[214:217], v248 offset:52224
	ds_read_b128 v[202:205], v248 offset:53248
	ds_read_b128 v[206:209], v248 offset:54272
	ds_read_b128 v[194:197], v248 offset:55296
	ds_read_b128 v[198:201], v248 offset:56320
	v_lshl_add_u64 v[238:239], v[238:239], 0, s[14:15]
	global_load_lds_dwordx4 v[238:239], off
	v_lshl_add_u64 v[236:237], v[236:237], 0, s[14:15]
	s_mov_b32 m0, s42
	s_and_b64 vcc, exec, s[2:3]
	global_load_lds_dwordx4 v[236:237], off
	s_waitcnt vmcnt(12)
	s_waitcnt lgkmcnt(0)
	s_barrier
	s_cbranch_vccnz .LBB0_4907
	s_setprio 1
	s_waitcnt lgkmcnt(0)
	v_mfma_f32_16x16x32_bf16 v[94:97], v[178:181], v[218:221], v[94:97]
	v_mfma_f32_16x16x32_bf16 v[90:93], v[186:189], v[218:221], v[90:93]
	v_mfma_f32_16x16x32_bf16 v[78:81], v[178:181], v[210:213], v[78:81]
	v_mfma_f32_16x16x32_bf16 v[74:77], v[186:189], v[210:213], v[74:77]
	v_mfma_f32_16x16x32_bf16 v[62:65], v[178:181], v[202:205], v[62:65]
	v_mfma_f32_16x16x32_bf16 v[58:61], v[186:189], v[202:205], v[58:61]
	v_mfma_f32_16x16x32_bf16 v[46:49], v[178:181], v[194:197], v[46:49]
	v_mfma_f32_16x16x32_bf16 v[42:45], v[186:189], v[194:197], v[42:45]
	v_mfma_f32_16x16x32_bf16 v[94:97], v[182:185], v[222:225], v[94:97]
	v_mfma_f32_16x16x32_bf16 v[90:93], v[190:193], v[222:225], v[90:93]
	v_mfma_f32_16x16x32_bf16 v[78:81], v[182:185], v[214:217], v[78:81]
	v_mfma_f32_16x16x32_bf16 v[74:77], v[190:193], v[214:217], v[74:77]
	v_mfma_f32_16x16x32_bf16 v[62:65], v[182:185], v[206:209], v[62:65]
	v_mfma_f32_16x16x32_bf16 v[58:61], v[190:193], v[206:209], v[58:61]
	v_mfma_f32_16x16x32_bf16 v[46:49], v[182:185], v[198:201], v[46:49]
	v_mfma_f32_16x16x32_bf16 v[42:45], v[190:193], v[198:201], v[42:45]
	s_setprio 0
	s_setprio 1
	v_mfma_f32_16x16x32_bf16 v[86:89], v[162:165], v[218:221], v[86:89]
	v_mfma_f32_16x16x32_bf16 v[82:85], v[170:173], v[218:221], v[82:85]
	v_mfma_f32_16x16x32_bf16 v[70:73], v[162:165], v[210:213], v[70:73]
	v_mfma_f32_16x16x32_bf16 v[66:69], v[170:173], v[210:213], v[66:69]
	v_mfma_f32_16x16x32_bf16 v[54:57], v[162:165], v[202:205], v[54:57]
	v_mfma_f32_16x16x32_bf16 v[50:53], v[170:173], v[202:205], v[50:53]
	v_mfma_f32_16x16x32_bf16 v[38:41], v[162:165], v[194:197], v[38:41]
	v_mfma_f32_16x16x32_bf16 v[34:37], v[170:173], v[194:197], v[34:37]
	v_mfma_f32_16x16x32_bf16 v[86:89], v[166:169], v[222:225], v[86:89]
	v_mfma_f32_16x16x32_bf16 v[82:85], v[174:177], v[222:225], v[82:85]
	v_mfma_f32_16x16x32_bf16 v[70:73], v[166:169], v[214:217], v[70:73]
	v_mfma_f32_16x16x32_bf16 v[66:69], v[174:177], v[214:217], v[66:69]
	v_mfma_f32_16x16x32_bf16 v[54:57], v[166:169], v[206:209], v[54:57]
	v_mfma_f32_16x16x32_bf16 v[50:53], v[174:177], v[206:209], v[50:53]
	v_mfma_f32_16x16x32_bf16 v[38:41], v[166:169], v[198:201], v[38:41]
	v_mfma_f32_16x16x32_bf16 v[34:37], v[174:177], v[198:201], v[34:37]
	s_setprio 0
	s_branch .LBB0_4907
